# GEMM main loops: per-segment s_setprio 1/0 toggling around the MFMA blocks removed (96 instructions); waves arbitrate by age only
# speedup vs baseline: 1.0083x; 1.0083x over previous
.LBB0_268:
	s_add_u32 s18, s8, s16
	s_addc_u32 s19, s9, s17
	s_add_u32 s20, s18, 0x100
	s_addc_u32 s21, s19, 0
	s_add_u32 s33, s42, s16
	s_addc_u32 s45, s43, s17
	s_cmpk_eq_i32 s16, 0x700
	s_cselect_b64 s[46:47], -1, 0
	s_and_b64 s[18:19], s[46:47], exec
	s_cselect_b32 s21, s9, s21
	s_cselect_b32 s20, s8, s20
	s_cselect_b32 s19, s13, s45
	s_cselect_b32 s18, s41, s33
	s_add_i32 s33, 0, 0x10000
	v_add_u32_e32 v135, s33, v148
	ds_read_b128 v[156:159], v135
	ds_read_b128 v[160:163], v135 offset:1024
	ds_read_b128 v[172:175], v135 offset:2048
	ds_read_b128 v[176:179], v135 offset:3072
	s_and_b64 vcc, s[6:7], s[46:47]
	v_cndmask_b32_e32 v226, v134, v152, vcc
	v_cndmask_b32_e32 v164, v136, v153, vcc
	v_cndmask_b32_e32 v135, v138, v154, vcc
	v_cndmask_b32_e32 v137, v140, v155, vcc
	v_lshl_add_u64 v[212:213], v[144:145], 0, s[16:17]
	s_add_i32 m0, s28, 0xc000
	ds_read_b128 v[180:183], v151
	ds_read_b128 v[184:187], v151 offset:1024
	ds_read_b128 v[188:191], v151 offset:2048
	ds_read_b128 v[192:195], v151 offset:3072
	ds_read_b128 v[196:199], v151 offset:4096
	ds_read_b128 v[200:203], v151 offset:5120
	ds_read_b128 v[204:207], v151 offset:6144
	ds_read_b128 v[208:211], v151 offset:7168
	global_load_lds_dwordx4 v[212:213], off
	v_lshl_add_u64 v[212:213], v[142:143], 0, s[16:17]
	s_add_i32 m0, s28, 0xe000
	s_nop 0
	global_load_lds_dwordx4 v[212:213], off
	s_waitcnt lgkmcnt(8)
	s_barrier
	s_waitcnt lgkmcnt(0)
	s_waitcnt lgkmcnt(0)
	v_mfma_f32_16x16x32_bf16 v[126:129], v[156:159], v[180:183], v[126:129]
	v_mfma_f32_16x16x32_bf16 v[122:125], v[172:175], v[180:183], v[122:125]
	v_mfma_f32_16x16x32_bf16 v[118:121], v[156:159], v[188:191], v[118:121]
	v_mfma_f32_16x16x32_bf16 v[110:113], v[172:175], v[188:191], v[110:113]
	v_mfma_f32_16x16x32_bf16 v[102:105], v[156:159], v[196:199], v[102:105]
	v_mfma_f32_16x16x32_bf16 v[94:97], v[172:175], v[196:199], v[94:97]
	v_mfma_f32_16x16x32_bf16 v[86:89], v[156:159], v[204:207], v[86:89]
	v_mfma_f32_16x16x32_bf16 v[78:81], v[172:175], v[204:207], v[78:81]
	v_mfma_f32_16x16x32_bf16 v[126:129], v[160:163], v[184:187], v[126:129]
	v_mfma_f32_16x16x32_bf16 v[122:125], v[176:179], v[184:187], v[122:125]
	v_mfma_f32_16x16x32_bf16 v[118:121], v[160:163], v[192:195], v[118:121]
	v_mfma_f32_16x16x32_bf16 v[110:113], v[176:179], v[192:195], v[110:113]
	v_mfma_f32_16x16x32_bf16 v[102:105], v[160:163], v[200:203], v[102:105]
	v_mfma_f32_16x16x32_bf16 v[94:97], v[176:179], v[200:203], v[94:97]
	v_mfma_f32_16x16x32_bf16 v[86:89], v[160:163], v[208:211], v[86:89]
	v_mfma_f32_16x16x32_bf16 v[78:81], v[176:179], v[208:211], v[78:81]
	s_barrier
	s_add_i32 s45, 0, 0x14000
	s_add_i32 s33, s33, s26
	v_add_u32_e32 v139, s45, v148
	v_lshl_add_u64 v[242:243], s[18:19], 0, v[132:133]
	s_mov_b32 m0, s33
	ds_read_b128 v[212:215], v139
	ds_read_b128 v[230:233], v139 offset:1024
	ds_read_b128 v[234:237], v139 offset:2048
	ds_read_b128 v[238:241], v139 offset:3072
	global_load_lds_dwordx4 v[242:243], off
	v_lshl_add_u64 v[244:245], s[18:19], 0, v[130:131]
	s_add_i32 m0, s33, 0x2000
	s_nop 0
	global_load_lds_dwordx4 v[244:245], off
	s_barrier
	s_waitcnt lgkmcnt(0)
	s_waitcnt lgkmcnt(0)
	v_mfma_f32_16x16x32_bf16 v[114:117], v[212:215], v[180:183], v[114:117]
	v_mfma_f32_16x16x32_bf16 v[106:109], v[234:237], v[180:183], v[106:109]
	v_mfma_f32_16x16x32_bf16 v[98:101], v[212:215], v[188:191], v[98:101]
	v_mfma_f32_16x16x32_bf16 v[90:93], v[234:237], v[188:191], v[90:93]
	v_mfma_f32_16x16x32_bf16 v[82:85], v[212:215], v[196:199], v[82:85]
	v_mfma_f32_16x16x32_bf16 v[74:77], v[234:237], v[196:199], v[74:77]
	v_mfma_f32_16x16x32_bf16 v[62:65], v[212:215], v[204:207], v[62:65]
	v_mfma_f32_16x16x32_bf16 v[58:61], v[234:237], v[204:207], v[58:61]
	v_mfma_f32_16x16x32_bf16 v[114:117], v[230:233], v[184:187], v[114:117]
	v_mfma_f32_16x16x32_bf16 v[106:109], v[238:241], v[184:187], v[106:109]
	v_mfma_f32_16x16x32_bf16 v[98:101], v[230:233], v[192:195], v[98:101]
	v_mfma_f32_16x16x32_bf16 v[90:93], v[238:241], v[192:195], v[90:93]
	v_mfma_f32_16x16x32_bf16 v[82:85], v[230:233], v[200:203], v[82:85]
	v_mfma_f32_16x16x32_bf16 v[74:77], v[238:241], v[200:203], v[74:77]
	v_mfma_f32_16x16x32_bf16 v[62:65], v[230:233], v[208:211], v[62:65]
	v_mfma_f32_16x16x32_bf16 v[58:61], v[238:241], v[208:211], v[58:61]
	s_mov_b32 m0, s28
	s_barrier
	ds_read_b128 v[180:183], v151 offset:16384
	ds_read_b128 v[184:187], v151 offset:17408
	ds_read_b128 v[188:191], v151 offset:18432
	ds_read_b128 v[192:195], v151 offset:19456
	ds_read_b128 v[196:199], v151 offset:20480
	ds_read_b128 v[200:203], v151 offset:21504
	ds_read_b128 v[204:207], v151 offset:22528
	ds_read_b128 v[208:211], v151 offset:23552
	global_load_lds_dwordx4 v226, s[20:21]
	s_mov_b32 m0, s29
	v_mov_b32_e32 v165, v227
	global_load_lds_dwordx4 v164, s[20:21]
	s_barrier
	s_waitcnt lgkmcnt(0)
	v_lshl_add_u64 v[246:247], s[20:21], 0, v[226:227]
	v_lshl_add_u64 v[164:165], s[20:21], 0, v[164:165]
	s_waitcnt lgkmcnt(0)
	v_mfma_f32_16x16x32_bf16 v[46:49], v[156:159], v[180:183], v[46:49]
	v_mfma_f32_16x16x32_bf16 v[34:37], v[172:175], v[180:183], v[34:37]
	v_mfma_f32_16x16x32_bf16 v[22:25], v[156:159], v[188:191], v[22:25]
	v_mfma_f32_16x16x32_bf16 v[18:21], v[172:175], v[188:191], v[18:21]
	v_mfma_f32_16x16x32_bf16 v[14:17], v[156:159], v[196:199], v[14:17]
	v_mfma_f32_16x16x32_bf16 v[10:13], v[172:175], v[196:199], v[10:13]
	v_mfma_f32_16x16x32_bf16 v[6:9], v[156:159], v[204:207], v[6:9]
	v_mfma_f32_16x16x32_bf16 v[2:5], v[172:175], v[204:207], v[2:5]
	v_mfma_f32_16x16x32_bf16 v[46:49], v[160:163], v[184:187], v[46:49]
	v_mfma_f32_16x16x32_bf16 v[34:37], v[176:179], v[184:187], v[34:37]
	v_mfma_f32_16x16x32_bf16 v[22:25], v[160:163], v[192:195], v[22:25]
	v_mfma_f32_16x16x32_bf16 v[18:21], v[176:179], v[192:195], v[18:21]
	v_mfma_f32_16x16x32_bf16 v[14:17], v[160:163], v[200:203], v[14:17]
	v_mfma_f32_16x16x32_bf16 v[10:13], v[176:179], v[200:203], v[10:13]
	v_mfma_f32_16x16x32_bf16 v[6:9], v[160:163], v[208:211], v[6:9]
	v_mfma_f32_16x16x32_bf16 v[2:5], v[176:179], v[208:211], v[2:5]
	s_barrier
	s_add_u32 s46, s18, 0x40000
	s_addc_u32 s47, s19, 0
	s_add_i32 s33, s45, s26
	v_lshl_add_u64 v[156:157], s[46:47], 0, v[132:133]
	s_mov_b32 m0, s33
	s_nop 0
	global_load_lds_dwordx4 v[156:157], off
	v_lshl_add_u64 v[156:157], s[46:47], 0, v[130:131]
	s_add_i32 m0, s33, 0x2000
	s_nop 0
	global_load_lds_dwordx4 v[156:157], off
	s_waitcnt vmcnt(6)
	s_barrier
	v_mfma_f32_16x16x32_bf16 v[70:73], v[212:215], v[180:183], v[70:73]
	v_mfma_f32_16x16x32_bf16 v[66:69], v[234:237], v[180:183], v[66:69]
	v_mfma_f32_16x16x32_bf16 v[54:57], v[212:215], v[188:191], v[54:57]
	v_mfma_f32_16x16x32_bf16 v[50:53], v[234:237], v[188:191], v[50:53]
	v_mfma_f32_16x16x32_bf16 v[42:45], v[212:215], v[196:199], v[42:45]
	v_mfma_f32_16x16x32_bf16 v[38:41], v[234:237], v[196:199], v[38:41]
	v_mfma_f32_16x16x32_bf16 v[30:33], v[212:215], v[204:207], v[30:33]
	v_mfma_f32_16x16x32_bf16 v[26:29], v[234:237], v[204:207], v[26:29]
	v_mfma_f32_16x16x32_bf16 v[70:73], v[230:233], v[184:187], v[70:73]
	v_mfma_f32_16x16x32_bf16 v[66:69], v[238:241], v[184:187], v[66:69]
	v_mfma_f32_16x16x32_bf16 v[54:57], v[230:233], v[192:195], v[54:57]
	v_mfma_f32_16x16x32_bf16 v[50:53], v[238:241], v[192:195], v[50:53]
	v_mfma_f32_16x16x32_bf16 v[42:45], v[230:233], v[200:203], v[42:45]
	v_mfma_f32_16x16x32_bf16 v[38:41], v[238:241], v[200:203], v[38:41]
	v_mfma_f32_16x16x32_bf16 v[30:33], v[230:233], v[208:211], v[30:33]
	v_mfma_f32_16x16x32_bf16 v[26:29], v[238:241], v[208:211], v[26:29]
	s_add_i32 s33, 0, 0x18000
	v_add_u32_e32 v139, s33, v148
	s_barrier
	ds_read_b128 v[156:159], v139
	ds_read_b128 v[160:163], v139 offset:1024
	ds_read_b128 v[172:175], v139 offset:2048
	ds_read_b128 v[176:179], v139 offset:3072
	s_mov_b32 m0, s30
	ds_read_b128 v[180:183], v151 offset:32768
	ds_read_b128 v[184:187], v151 offset:33792
	ds_read_b128 v[188:191], v151 offset:34816
	ds_read_b128 v[192:195], v151 offset:35840
	ds_read_b128 v[196:199], v151 offset:36864
	ds_read_b128 v[200:203], v151 offset:37888
	ds_read_b128 v[204:207], v151 offset:38912
	ds_read_b128 v[208:211], v151 offset:39936
	global_load_lds_dwordx4 v135, s[20:21]
	s_mov_b32 m0, s31
	s_nop 0
	global_load_lds_dwordx4 v137, s[20:21]
	s_waitcnt lgkmcnt(8)
	s_barrier
	s_waitcnt lgkmcnt(0)
	s_waitcnt lgkmcnt(0)
	v_mfma_f32_16x16x32_bf16 v[126:129], v[156:159], v[180:183], v[126:129]
	v_mfma_f32_16x16x32_bf16 v[122:125], v[172:175], v[180:183], v[122:125]
	v_mfma_f32_16x16x32_bf16 v[118:121], v[156:159], v[188:191], v[118:121]
	v_mfma_f32_16x16x32_bf16 v[110:113], v[172:175], v[188:191], v[110:113]
	v_mfma_f32_16x16x32_bf16 v[102:105], v[156:159], v[196:199], v[102:105]
	v_mfma_f32_16x16x32_bf16 v[94:97], v[172:175], v[196:199], v[94:97]
	v_mfma_f32_16x16x32_bf16 v[86:89], v[156:159], v[204:207], v[86:89]
	v_mfma_f32_16x16x32_bf16 v[78:81], v[172:175], v[204:207], v[78:81]
	v_mfma_f32_16x16x32_bf16 v[126:129], v[160:163], v[184:187], v[126:129]
	v_mfma_f32_16x16x32_bf16 v[122:125], v[176:179], v[184:187], v[122:125]
	v_mfma_f32_16x16x32_bf16 v[118:121], v[160:163], v[192:195], v[118:121]
	v_mfma_f32_16x16x32_bf16 v[110:113], v[176:179], v[192:195], v[110:113]
	v_mfma_f32_16x16x32_bf16 v[102:105], v[160:163], v[200:203], v[102:105]
	v_mfma_f32_16x16x32_bf16 v[94:97], v[176:179], v[200:203], v[94:97]
	v_mfma_f32_16x16x32_bf16 v[86:89], v[160:163], v[208:211], v[86:89]
	v_mfma_f32_16x16x32_bf16 v[78:81], v[176:179], v[208:211], v[78:81]
	s_barrier
	s_add_i32 s20, 0, 0x1c000
	s_add_i32 s21, s33, s26
	v_add_u32_e32 v135, s20, v148
	v_lshl_add_u64 v[242:243], v[242:243], 0, s[96:97]
	s_mov_b32 m0, s21
	ds_read_b128 v[212:215], v135
	ds_read_b128 v[230:233], v135 offset:1024
	ds_read_b128 v[234:237], v135 offset:2048
	ds_read_b128 v[238:241], v135 offset:3072
	global_load_lds_dwordx4 v[242:243], off
	v_lshl_add_u64 v[242:243], v[244:245], 0, s[96:97]
	s_add_i32 m0, s21, 0x2000
	s_nop 0
	global_load_lds_dwordx4 v[242:243], off
	s_barrier
	s_waitcnt lgkmcnt(0)
	s_waitcnt lgkmcnt(0)
	v_mfma_f32_16x16x32_bf16 v[114:117], v[212:215], v[180:183], v[114:117]
	v_mfma_f32_16x16x32_bf16 v[106:109], v[234:237], v[180:183], v[106:109]
	v_mfma_f32_16x16x32_bf16 v[98:101], v[212:215], v[188:191], v[98:101]
	v_mfma_f32_16x16x32_bf16 v[90:93], v[234:237], v[188:191], v[90:93]
	v_mfma_f32_16x16x32_bf16 v[82:85], v[212:215], v[196:199], v[82:85]
	v_mfma_f32_16x16x32_bf16 v[74:77], v[234:237], v[196:199], v[74:77]
	v_mfma_f32_16x16x32_bf16 v[62:65], v[212:215], v[204:207], v[62:65]
	v_mfma_f32_16x16x32_bf16 v[58:61], v[234:237], v[204:207], v[58:61]
	v_mfma_f32_16x16x32_bf16 v[114:117], v[230:233], v[184:187], v[114:117]
	v_mfma_f32_16x16x32_bf16 v[106:109], v[238:241], v[184:187], v[106:109]
	v_mfma_f32_16x16x32_bf16 v[98:101], v[230:233], v[192:195], v[98:101]
	v_mfma_f32_16x16x32_bf16 v[90:93], v[238:241], v[192:195], v[90:93]
	v_mfma_f32_16x16x32_bf16 v[82:85], v[230:233], v[200:203], v[82:85]
	v_mfma_f32_16x16x32_bf16 v[74:77], v[238:241], v[200:203], v[74:77]
	v_mfma_f32_16x16x32_bf16 v[62:65], v[230:233], v[208:211], v[62:65]
	v_mfma_f32_16x16x32_bf16 v[58:61], v[238:241], v[208:211], v[58:61]
	s_mov_b32 m0, s34
	v_lshl_add_u64 v[242:243], v[246:247], 0, s[96:97]
	s_barrier
	ds_read_b128 v[180:183], v151 offset:49152
	ds_read_b128 v[184:187], v151 offset:50176
	ds_read_b128 v[188:191], v151 offset:51200
	ds_read_b128 v[192:195], v151 offset:52224
	ds_read_b128 v[196:199], v151 offset:53248
	ds_read_b128 v[200:203], v151 offset:54272
	ds_read_b128 v[204:207], v151 offset:55296
	ds_read_b128 v[208:211], v151 offset:56320
	global_load_lds_dwordx4 v[242:243], off
	v_lshl_add_u64 v[164:165], v[164:165], 0, s[96:97]
	s_mov_b32 m0, s35
	s_nop 0
	global_load_lds_dwordx4 v[164:165], off
	s_barrier
	s_waitcnt lgkmcnt(0)
	s_waitcnt lgkmcnt(0)
	v_mfma_f32_16x16x32_bf16 v[46:49], v[156:159], v[180:183], v[46:49]
	v_mfma_f32_16x16x32_bf16 v[34:37], v[172:175], v[180:183], v[34:37]
	v_mfma_f32_16x16x32_bf16 v[22:25], v[156:159], v[188:191], v[22:25]
	v_mfma_f32_16x16x32_bf16 v[18:21], v[172:175], v[188:191], v[18:21]
	v_mfma_f32_16x16x32_bf16 v[14:17], v[156:159], v[196:199], v[14:17]
	v_mfma_f32_16x16x32_bf16 v[10:13], v[172:175], v[196:199], v[10:13]
	v_mfma_f32_16x16x32_bf16 v[6:9], v[156:159], v[204:207], v[6:9]
	v_mfma_f32_16x16x32_bf16 v[2:5], v[172:175], v[204:207], v[2:5]
	v_mfma_f32_16x16x32_bf16 v[46:49], v[160:163], v[184:187], v[46:49]
	v_mfma_f32_16x16x32_bf16 v[34:37], v[176:179], v[184:187], v[34:37]
	v_mfma_f32_16x16x32_bf16 v[22:25], v[160:163], v[192:195], v[22:25]
	v_mfma_f32_16x16x32_bf16 v[18:21], v[176:179], v[192:195], v[18:21]
	v_mfma_f32_16x16x32_bf16 v[14:17], v[160:163], v[200:203], v[14:17]
	v_mfma_f32_16x16x32_bf16 v[10:13], v[176:179], v[200:203], v[10:13]
	v_mfma_f32_16x16x32_bf16 v[6:9], v[160:163], v[208:211], v[6:9]
	v_mfma_f32_16x16x32_bf16 v[2:5], v[176:179], v[208:211], v[2:5]
	s_barrier
	s_add_u32 s18, s18, 0x40080
	s_addc_u32 s19, s19, 0
	s_add_i32 s20, s20, s26
	v_lshl_add_u64 v[156:157], s[18:19], 0, v[132:133]
	s_mov_b32 m0, s20
	s_nop 0
	global_load_lds_dwordx4 v[156:157], off
	v_lshl_add_u64 v[156:157], s[18:19], 0, v[130:131]
	s_add_i32 m0, s20, 0x2000
	s_nop 0
	global_load_lds_dwordx4 v[156:157], off
	s_waitcnt vmcnt(6)
	s_barrier
	v_mfma_f32_16x16x32_bf16 v[70:73], v[212:215], v[180:183], v[70:73]
	v_mfma_f32_16x16x32_bf16 v[66:69], v[234:237], v[180:183], v[66:69]
	v_mfma_f32_16x16x32_bf16 v[54:57], v[212:215], v[188:191], v[54:57]
	v_mfma_f32_16x16x32_bf16 v[50:53], v[234:237], v[188:191], v[50:53]
	v_mfma_f32_16x16x32_bf16 v[42:45], v[212:215], v[196:199], v[42:45]
	v_mfma_f32_16x16x32_bf16 v[38:41], v[234:237], v[196:199], v[38:41]
	v_mfma_f32_16x16x32_bf16 v[30:33], v[212:215], v[204:207], v[30:33]
	v_mfma_f32_16x16x32_bf16 v[26:29], v[234:237], v[204:207], v[26:29]
	v_mfma_f32_16x16x32_bf16 v[70:73], v[230:233], v[184:187], v[70:73]
	v_mfma_f32_16x16x32_bf16 v[66:69], v[238:241], v[184:187], v[66:69]
	v_mfma_f32_16x16x32_bf16 v[54:57], v[230:233], v[192:195], v[54:57]
	v_mfma_f32_16x16x32_bf16 v[50:53], v[238:241], v[192:195], v[50:53]
	v_mfma_f32_16x16x32_bf16 v[42:45], v[230:233], v[200:203], v[42:45]
	v_mfma_f32_16x16x32_bf16 v[38:41], v[238:241], v[200:203], v[38:41]
	v_mfma_f32_16x16x32_bf16 v[30:33], v[230:233], v[208:211], v[30:33]
	v_mfma_f32_16x16x32_bf16 v[26:29], v[238:241], v[208:211], v[26:29]
	s_add_i32 s44, s44, 2
	s_add_u32 s16, s16, 0x100
	s_addc_u32 s17, s17, 0
	s_cmp_gt_u32 s44, 13
	s_barrier
	s_cbranch_scc0 .LBB0_268
	v_lshl_or_b32 v136, s40, 8, v150
	v_lshl_add_u32 v140, s39, 8, v147
	v_ashrrev_i32_e32 v137, 31, v136
	v_mov_b64_e32 v[134:135], s[10:11]
	s_movk_i32 s13, 0x1c00
	v_mad_i64_i32 v[138:139], s[6:7], v140, s13, v[134:135]
	v_lshlrev_b64 v[136:137], 1, v[136:137]
	v_lshl_add_u64 v[138:139], v[138:139], 0, v[136:137]
	v_cvt_pk_bf16_f32 v126, v126, v127
	v_cvt_pk_bf16_f32 v127, v128, v129
	v_cvt_pk_bf16_f32 v128, v122, v123
	v_cvt_pk_bf16_f32 v129, v124, v125
	global_store_dwordx4 v[138:139], v[126:129], off
	v_cvt_pk_bf16_f32 v114, v114, v115
	v_cvt_pk_bf16_f32 v115, v116, v117
	v_cvt_pk_bf16_f32 v116, v106, v107
	v_or_b32_e32 v106, 16, v140
	v_mad_i64_i32 v[106:107], s[6:7], v106, s13, v[134:135]
	v_cvt_pk_bf16_f32 v117, v108, v109
	global_store_dwordx4 v[138:139], v[114:117], off offset:256
	s_and_b64 vcc, exec, s[4:5]
	v_mov_b32_e32 v138, v154
	v_lshl_add_u64 v[114:115], v[106:107], 0, v[136:137]
	v_cvt_pk_bf16_f32 v106, v118, v119
	v_cvt_pk_bf16_f32 v107, v120, v121
	v_cvt_pk_bf16_f32 v108, v110, v111
	v_cvt_pk_bf16_f32 v109, v112, v113
	global_store_dwordx4 v[114:115], v[106:109], off
	v_cvt_pk_bf16_f32 v98, v98, v99
	v_cvt_pk_bf16_f32 v99, v100, v101
	v_cvt_pk_bf16_f32 v100, v90, v91
	v_or_b32_e32 v90, 32, v140
	v_mad_i64_i32 v[90:91], s[6:7], v90, s13, v[134:135]
	v_cvt_pk_bf16_f32 v101, v92, v93
	global_store_dwordx4 v[114:115], v[98:101], off offset:256
	s_mov_b32 s40, s12
	s_mov_b32 s39, s38
	v_lshl_add_u64 v[98:99], v[90:91], 0, v[136:137]
	v_cvt_pk_bf16_f32 v90, v102, v103
	v_cvt_pk_bf16_f32 v91, v104, v105
	v_cvt_pk_bf16_f32 v92, v94, v95
	v_cvt_pk_bf16_f32 v93, v96, v97
	global_store_dwordx4 v[98:99], v[90:93], off
	v_cvt_pk_bf16_f32 v82, v82, v83
	v_cvt_pk_bf16_f32 v83, v84, v85
	v_cvt_pk_bf16_f32 v84, v74, v75
	v_or_b32_e32 v74, 48, v140
	v_mad_i64_i32 v[74:75], s[6:7], v74, s13, v[134:135]
	v_cvt_pk_bf16_f32 v85, v76, v77
	global_store_dwordx4 v[98:99], v[82:85], off offset:256
	s_mov_b64 s[16:17], s[14:15]
	s_nop 0
	v_lshl_add_u64 v[82:83], v[74:75], 0, v[136:137]
	v_cvt_pk_bf16_f32 v74, v86, v87
	v_cvt_pk_bf16_f32 v75, v88, v89
	v_cvt_pk_bf16_f32 v76, v78, v79
	v_cvt_pk_bf16_f32 v77, v80, v81
	global_store_dwordx4 v[82:83], v[74:77], off
	v_cvt_pk_bf16_f32 v62, v62, v63
	v_cvt_pk_bf16_f32 v63, v64, v65
	v_cvt_pk_bf16_f32 v64, v58, v59
	v_add_u32_e32 v58, 0x80, v140
	v_mad_i64_i32 v[58:59], s[6:7], v58, s13, v[134:135]
	v_lshl_add_u64 v[58:59], v[58:59], 0, v[136:137]
	v_cvt_pk_bf16_f32 v65, v60, v61
	global_store_dwordx4 v[82:83], v[62:65], off offset:256
	v_cvt_pk_bf16_f32 v46, v46, v47
	v_cvt_pk_bf16_f32 v47, v48, v49
	v_cvt_pk_bf16_f32 v48, v34, v35
	v_cvt_pk_bf16_f32 v49, v36, v37
	global_store_dwordx4 v[58:59], v[46:49], off
	v_cvt_pk_bf16_f32 v34, v70, v71
	v_cvt_pk_bf16_f32 v35, v72, v73
	v_cvt_pk_bf16_f32 v36, v66, v67
	v_cvt_pk_bf16_f32 v37, v68, v69
	global_store_dwordx4 v[58:59], v[34:37], off offset:256
	v_cvt_pk_bf16_f32 v22, v22, v23
	v_cvt_pk_bf16_f32 v23, v24, v25
	v_cvt_pk_bf16_f32 v24, v18, v19
	v_cvt_pk_bf16_f32 v25, v20, v21
	s_nop 1
	v_add_u32_e32 v34, 0x90, v140
	v_mad_i64_i32 v[34:35], s[6:7], v34, s13, v[134:135]
	v_lshl_add_u64 v[34:35], v[34:35], 0, v[136:137]
	global_store_dwordx4 v[34:35], v[22:25], off
	v_cvt_pk_bf16_f32 v18, v54, v55
	v_cvt_pk_bf16_f32 v19, v56, v57
	v_cvt_pk_bf16_f32 v20, v50, v51
	v_cvt_pk_bf16_f32 v21, v52, v53
	global_store_dwordx4 v[34:35], v[18:21], off offset:256
	v_cvt_pk_bf16_f32 v14, v14, v15
	v_cvt_pk_bf16_f32 v15, v16, v17
	v_cvt_pk_bf16_f32 v16, v10, v11
	v_cvt_pk_bf16_f32 v17, v12, v13
	s_nop 1
	v_add_u32_e32 v18, 0xa0, v140
	v_mad_i64_i32 v[18:19], s[6:7], v18, s13, v[134:135]
	v_lshl_add_u64 v[18:19], v[18:19], 0, v[136:137]
	global_store_dwordx4 v[18:19], v[14:17], off
	v_cvt_pk_bf16_f32 v10, v42, v43
	v_cvt_pk_bf16_f32 v11, v44, v45
	v_cvt_pk_bf16_f32 v12, v38, v39
	v_cvt_pk_bf16_f32 v13, v40, v41
	global_store_dwordx4 v[18:19], v[10:13], off offset:256
	v_cvt_pk_bf16_f32 v6, v6, v7
	v_cvt_pk_bf16_f32 v7, v8, v9
	v_cvt_pk_bf16_f32 v8, v2, v3
	v_cvt_pk_bf16_f32 v9, v4, v5
	s_nop 1
	v_add_u32_e32 v10, 0xb0, v140
	v_mad_i64_i32 v[10:11], s[6:7], v10, s13, v[134:135]
	v_lshl_add_u64 v[10:11], v[10:11], 0, v[136:137]
	v_mov_b32_e32 v140, v155
	v_mov_b32_e32 v136, v153
	v_mov_b32_e32 v134, v152
	global_store_dwordx4 v[10:11], v[6:9], off
	v_cvt_pk_bf16_f32 v2, v30, v31
	v_cvt_pk_bf16_f32 v3, v32, v33
	v_cvt_pk_bf16_f32 v4, v26, v27
	v_cvt_pk_bf16_f32 v5, v28, v29
	global_store_dwordx4 v[10:11], v[2:5], off offset:256
	s_cbranch_vccz .LBB0_265
	s_waitcnt vmcnt(0)
	s_cmpk_gt_u32 s23, 0xff
	s_cbranch_scc1 .LBB0_272
	s_barrier

.LBB0_423:
	s_add_i32 s36, 0, 0x10000
	v_add_u32_e32 v39, s36, v51
	ds_read_b128 v[10:13], v39
	ds_read_b128 v[14:17], v39 offset:1024
	ds_read_b128 v[18:21], v39 offset:2048
	ds_read_b128 v[22:25], v39 offset:3072
	v_lshl_add_u64 v[8:9], s[12:13], 0, v[226:227]
	s_add_i32 s35, s20, 0xc000
	v_mov_b32_e32 v7, v227
	v_lshl_add_u64 v[76:77], v[8:9], 0, s[96:97]
	s_mov_b32 m0, s35
	v_lshl_add_u64 v[6:7], s[12:13], 0, v[6:7]
	s_add_i32 s8, s20, 0xe000
	ds_read_b128 v[26:29], v53
	ds_read_b128 v[30:33], v53 offset:1024
	ds_read_b128 v[42:45], v53 offset:2048
	ds_read_b128 v[56:59], v53 offset:3072
	ds_read_b128 v[60:63], v53 offset:4096
	ds_read_b128 v[64:67], v53 offset:5120
	ds_read_b128 v[68:71], v53 offset:6144
	ds_read_b128 v[72:75], v53 offset:7168
	global_load_lds_dwordx4 v[76:77], off
	v_lshl_add_u64 v[76:77], v[6:7], 0, s[96:97]
	s_mov_b32 m0, s8
	s_nop 0
	global_load_lds_dwordx4 v[76:77], off
	s_waitcnt lgkmcnt(8)
	s_barrier
	s_waitcnt lgkmcnt(0)
	s_waitcnt lgkmcnt(0)
	v_mfma_f32_16x16x32_bf16 v[76:79], v[10:13], v[26:29], 0
	v_mfma_f32_16x16x32_bf16 v[80:83], v[18:21], v[26:29], 0
	v_mfma_f32_16x16x32_bf16 v[84:87], v[10:13], v[42:45], 0
	v_mfma_f32_16x16x32_bf16 v[88:91], v[18:21], v[42:45], 0
	v_mfma_f32_16x16x32_bf16 v[92:95], v[10:13], v[60:63], 0
	v_mfma_f32_16x16x32_bf16 v[96:99], v[18:21], v[60:63], 0
	v_mfma_f32_16x16x32_bf16 v[100:103], v[10:13], v[68:71], 0
	v_mfma_f32_16x16x32_bf16 v[104:107], v[18:21], v[68:71], 0
	v_mfma_f32_16x16x32_bf16 v[76:79], v[14:17], v[30:33], v[76:79]
	v_mfma_f32_16x16x32_bf16 v[80:83], v[22:25], v[30:33], v[80:83]
	v_mfma_f32_16x16x32_bf16 v[84:87], v[14:17], v[56:59], v[84:87]
	v_mfma_f32_16x16x32_bf16 v[88:91], v[22:25], v[56:59], v[88:91]
	v_mfma_f32_16x16x32_bf16 v[92:95], v[14:17], v[64:67], v[92:95]
	v_mfma_f32_16x16x32_bf16 v[96:99], v[22:25], v[64:67], v[96:99]
	v_mfma_f32_16x16x32_bf16 v[100:103], v[14:17], v[72:75], v[100:103]
	v_mfma_f32_16x16x32_bf16 v[104:107], v[22:25], v[72:75], v[104:107]
	s_barrier
	s_add_i32 s37, 0, 0x14000
	v_lshl_add_u64 v[164:165], s[14:15], 0, v[36:37]
	s_mov_b64 s[40:41], 0x100
	s_add_i32 s36, s36, s19
	v_add_u32_e32 v41, s37, v51
	v_lshl_add_u64 v[124:125], v[164:165], 0, s[40:41]
	s_mov_b32 m0, s36
	v_lshl_add_u64 v[238:239], s[14:15], 0, v[34:35]
	s_add_i32 s34, s36, 0x2000
	ds_read_b128 v[108:111], v41
	ds_read_b128 v[112:115], v41 offset:1024
	ds_read_b128 v[116:119], v41 offset:2048
	ds_read_b128 v[120:123], v41 offset:3072
	global_load_lds_dwordx4 v[124:125], off
	v_lshl_add_u64 v[124:125], v[238:239], 0, s[40:41]
	s_mov_b32 m0, s34
	s_nop 0
	global_load_lds_dwordx4 v[124:125], off
	s_barrier
	s_waitcnt lgkmcnt(0)
	s_waitcnt lgkmcnt(0)
	v_mfma_f32_16x16x32_bf16 v[124:127], v[108:111], v[26:29], 0
	v_mfma_f32_16x16x32_bf16 v[26:29], v[116:119], v[26:29], 0
	v_mfma_f32_16x16x32_bf16 v[124:127], v[112:115], v[30:33], v[124:127]
	v_mfma_f32_16x16x32_bf16 v[26:29], v[120:123], v[30:33], v[26:29]
	v_mfma_f32_16x16x32_bf16 v[30:33], v[108:111], v[42:45], 0
	v_mfma_f32_16x16x32_bf16 v[42:45], v[116:119], v[42:45], 0
	v_mfma_f32_16x16x32_bf16 v[30:33], v[112:115], v[56:59], v[30:33]
	v_mfma_f32_16x16x32_bf16 v[42:45], v[120:123], v[56:59], v[42:45]
	v_mfma_f32_16x16x32_bf16 v[56:59], v[108:111], v[60:63], 0
	v_mfma_f32_16x16x32_bf16 v[60:63], v[116:119], v[60:63], 0
	v_mfma_f32_16x16x32_bf16 v[56:59], v[112:115], v[64:67], v[56:59]
	v_mfma_f32_16x16x32_bf16 v[60:63], v[120:123], v[64:67], v[60:63]
	v_mfma_f32_16x16x32_bf16 v[64:67], v[108:111], v[68:71], 0
	v_mfma_f32_16x16x32_bf16 v[68:71], v[116:119], v[68:71], 0
	v_mfma_f32_16x16x32_bf16 v[64:67], v[112:115], v[72:75], v[64:67]
	v_mfma_f32_16x16x32_bf16 v[68:71], v[120:123], v[72:75], v[68:71]
	v_mov_b32_e32 v5, v227
	v_lshl_add_u64 v[240:241], s[12:13], 0, v[4:5]
	v_mov_b32_e32 v3, v227
	s_mov_b32 m0, s20
	v_lshl_add_u64 v[4:5], v[240:241], 0, s[40:41]
	v_lshl_add_u64 v[242:243], s[12:13], 0, v[2:3]
	s_barrier
	ds_read_b128 v[72:75], v53 offset:16384
	ds_read_b128 v[128:131], v53 offset:17408
	ds_read_b128 v[132:135], v53 offset:18432
	ds_read_b128 v[136:139], v53 offset:19456
	ds_read_b128 v[140:143], v53 offset:20480
	ds_read_b128 v[144:147], v53 offset:21504
	ds_read_b128 v[148:151], v53 offset:22528
	ds_read_b128 v[152:155], v53 offset:23552
	global_load_lds_dwordx4 v[4:5], off
	v_lshl_add_u64 v[2:3], v[242:243], 0, s[40:41]
	s_mov_b32 m0, s21
	s_nop 0
	global_load_lds_dwordx4 v[2:3], off
	s_barrier
	s_waitcnt lgkmcnt(0)
	s_waitcnt lgkmcnt(0)
	v_mfma_f32_16x16x32_bf16 v[2:5], v[10:13], v[72:75], 0
	v_mfma_f32_16x16x32_bf16 v[160:163], v[10:13], v[132:135], 0
	v_mfma_f32_16x16x32_bf16 v[176:179], v[10:13], v[140:143], 0
	v_mfma_f32_16x16x32_bf16 v[10:13], v[10:13], v[148:151], 0
	v_mfma_f32_16x16x32_bf16 v[2:5], v[14:17], v[128:131], v[2:5]
	v_mfma_f32_16x16x32_bf16 v[156:159], v[18:21], v[72:75], 0
	v_mfma_f32_16x16x32_bf16 v[160:163], v[14:17], v[136:139], v[160:163]
	v_mfma_f32_16x16x32_bf16 v[172:175], v[18:21], v[132:135], 0
	v_mfma_f32_16x16x32_bf16 v[176:179], v[14:17], v[144:147], v[176:179]
	v_mfma_f32_16x16x32_bf16 v[180:183], v[18:21], v[140:143], 0
	v_mfma_f32_16x16x32_bf16 v[10:13], v[14:17], v[152:155], v[10:13]
	v_mfma_f32_16x16x32_bf16 v[14:17], v[18:21], v[148:151], 0
	v_mfma_f32_16x16x32_bf16 v[156:159], v[22:25], v[128:131], v[156:159]
	v_mfma_f32_16x16x32_bf16 v[172:175], v[22:25], v[136:139], v[172:175]
	v_mfma_f32_16x16x32_bf16 v[180:183], v[22:25], v[144:147], v[180:183]
	v_mfma_f32_16x16x32_bf16 v[14:17], v[22:25], v[152:155], v[14:17]
	s_barrier
	s_add_u32 s38, s14, 0x18100
	s_addc_u32 s39, s15, 0
	s_add_i32 s37, s37, s19
	v_lshl_add_u64 v[18:19], s[38:39], 0, v[36:37]
	s_mov_b32 m0, s37
	s_add_i32 s9, s37, 0x2000
	global_load_lds_dwordx4 v[18:19], off
	v_lshl_add_u64 v[18:19], s[38:39], 0, v[34:35]
	s_mov_b32 m0, s9
	s_nop 0
	global_load_lds_dwordx4 v[18:19], off
	s_waitcnt vmcnt(6)
	s_barrier
	v_mfma_f32_16x16x32_bf16 v[18:21], v[108:111], v[72:75], 0
	v_mfma_f32_16x16x32_bf16 v[22:25], v[116:119], v[72:75], 0
	v_mfma_f32_16x16x32_bf16 v[18:21], v[112:115], v[128:131], v[18:21]
	v_mfma_f32_16x16x32_bf16 v[22:25], v[120:123], v[128:131], v[22:25]
	v_mfma_f32_16x16x32_bf16 v[72:75], v[108:111], v[132:135], 0
	v_mfma_f32_16x16x32_bf16 v[128:131], v[116:119], v[132:135], 0
	v_mfma_f32_16x16x32_bf16 v[132:135], v[108:111], v[140:143], 0
	v_mfma_f32_16x16x32_bf16 v[108:111], v[108:111], v[148:151], 0
	v_mfma_f32_16x16x32_bf16 v[72:75], v[112:115], v[136:139], v[72:75]
	v_mfma_f32_16x16x32_bf16 v[128:131], v[120:123], v[136:139], v[128:131]
	v_mfma_f32_16x16x32_bf16 v[132:135], v[112:115], v[144:147], v[132:135]
	v_mfma_f32_16x16x32_bf16 v[136:139], v[116:119], v[140:143], 0
	v_mfma_f32_16x16x32_bf16 v[108:111], v[112:115], v[152:155], v[108:111]
	v_mfma_f32_16x16x32_bf16 v[112:115], v[116:119], v[148:151], 0
	v_mfma_f32_16x16x32_bf16 v[136:139], v[120:123], v[144:147], v[136:139]
	v_mfma_f32_16x16x32_bf16 v[112:115], v[120:123], v[152:155], v[112:115]
	s_add_i32 s39, 0, 0x18000
	v_add_u32_e32 v166, s39, v51
	s_barrier
	ds_read_b128 v[116:119], v166
	ds_read_b128 v[120:123], v166 offset:1024
	ds_read_b128 v[140:143], v166 offset:2048
	ds_read_b128 v[144:147], v166 offset:3072
	s_mov_b32 m0, s22
	v_lshl_add_u64 v[208:209], v[8:9], 0, s[40:41]
	ds_read_b128 v[148:151], v53 offset:32768
	ds_read_b128 v[152:155], v53 offset:33792
	ds_read_b128 v[184:187], v53 offset:34816
	ds_read_b128 v[188:191], v53 offset:35840
	ds_read_b128 v[192:195], v53 offset:36864
	ds_read_b128 v[196:199], v53 offset:37888
	ds_read_b128 v[200:203], v53 offset:38912
	ds_read_b128 v[204:207], v53 offset:39936
	global_load_lds_dwordx4 v[208:209], off
	v_lshl_add_u64 v[208:209], v[6:7], 0, s[40:41]
	s_mov_b32 m0, s23
	s_nop 0
	global_load_lds_dwordx4 v[208:209], off
	s_waitcnt lgkmcnt(8)
	s_barrier
	s_waitcnt lgkmcnt(0)
	s_waitcnt lgkmcnt(0)
	v_mfma_f32_16x16x32_bf16 v[76:79], v[116:119], v[148:151], v[76:79]
	v_mfma_f32_16x16x32_bf16 v[80:83], v[140:143], v[148:151], v[80:83]
	v_mfma_f32_16x16x32_bf16 v[84:87], v[116:119], v[184:187], v[84:87]
	v_mfma_f32_16x16x32_bf16 v[88:91], v[140:143], v[184:187], v[88:91]
	v_mfma_f32_16x16x32_bf16 v[92:95], v[116:119], v[192:195], v[92:95]
	v_mfma_f32_16x16x32_bf16 v[96:99], v[140:143], v[192:195], v[96:99]
	v_mfma_f32_16x16x32_bf16 v[100:103], v[116:119], v[200:203], v[100:103]
	v_mfma_f32_16x16x32_bf16 v[104:107], v[140:143], v[200:203], v[104:107]
	v_mfma_f32_16x16x32_bf16 v[76:79], v[120:123], v[152:155], v[76:79]
	v_mfma_f32_16x16x32_bf16 v[80:83], v[144:147], v[152:155], v[80:83]
	v_mfma_f32_16x16x32_bf16 v[84:87], v[120:123], v[188:191], v[84:87]
	v_mfma_f32_16x16x32_bf16 v[88:91], v[144:147], v[188:191], v[88:91]
	v_mfma_f32_16x16x32_bf16 v[92:95], v[120:123], v[196:199], v[92:95]
	v_mfma_f32_16x16x32_bf16 v[96:99], v[144:147], v[196:199], v[96:99]
	v_mfma_f32_16x16x32_bf16 v[100:103], v[120:123], v[204:207], v[100:103]
	v_mfma_f32_16x16x32_bf16 v[104:107], v[144:147], v[204:207], v[104:107]
	s_barrier
	s_add_i32 s33, 0, 0x1c000
	s_mov_b64 s[46:47], 0x180
	s_add_i32 s39, s39, s19
	v_add_u32_e32 v167, s33, v51
	v_lshl_add_u64 v[164:165], v[164:165], 0, s[46:47]
	s_mov_b32 m0, s39
	s_add_i32 s38, s39, 0x2000
	ds_read_b128 v[208:211], v167
	ds_read_b128 v[212:215], v167 offset:1024
	ds_read_b128 v[230:233], v167 offset:2048
	ds_read_b128 v[234:237], v167 offset:3072
	global_load_lds_dwordx4 v[164:165], off
	v_lshl_add_u64 v[164:165], v[238:239], 0, s[46:47]
	s_mov_b32 m0, s38
	s_nop 0
	global_load_lds_dwordx4 v[164:165], off
	s_barrier
	s_waitcnt lgkmcnt(0)
	s_waitcnt lgkmcnt(0)
	v_mfma_f32_16x16x32_bf16 v[124:127], v[208:211], v[148:151], v[124:127]
	v_mfma_f32_16x16x32_bf16 v[26:29], v[230:233], v[148:151], v[26:29]
	v_mfma_f32_16x16x32_bf16 v[30:33], v[208:211], v[184:187], v[30:33]
	v_mfma_f32_16x16x32_bf16 v[42:45], v[230:233], v[184:187], v[42:45]
	v_mfma_f32_16x16x32_bf16 v[56:59], v[208:211], v[192:195], v[56:59]
	v_mfma_f32_16x16x32_bf16 v[60:63], v[230:233], v[192:195], v[60:63]
	v_mfma_f32_16x16x32_bf16 v[64:67], v[208:211], v[200:203], v[64:67]
	v_mfma_f32_16x16x32_bf16 v[68:71], v[230:233], v[200:203], v[68:71]
	v_mfma_f32_16x16x32_bf16 v[124:127], v[212:215], v[152:155], v[124:127]
	v_mfma_f32_16x16x32_bf16 v[26:29], v[234:237], v[152:155], v[26:29]
	v_mfma_f32_16x16x32_bf16 v[30:33], v[212:215], v[188:191], v[30:33]
	v_mfma_f32_16x16x32_bf16 v[42:45], v[234:237], v[188:191], v[42:45]
	v_mfma_f32_16x16x32_bf16 v[56:59], v[212:215], v[196:199], v[56:59]
	v_mfma_f32_16x16x32_bf16 v[60:63], v[234:237], v[196:199], v[60:63]
	v_mfma_f32_16x16x32_bf16 v[64:67], v[212:215], v[204:207], v[64:67]
	v_mfma_f32_16x16x32_bf16 v[68:71], v[234:237], v[204:207], v[68:71]
	s_mov_b32 m0, s24
	v_lshl_add_u64 v[164:165], v[240:241], 0, s[46:47]
	s_barrier
	ds_read_b128 v[148:151], v53 offset:49152
	ds_read_b128 v[152:155], v53 offset:50176
	ds_read_b128 v[184:187], v53 offset:51200
	ds_read_b128 v[188:191], v53 offset:52224
	ds_read_b128 v[192:195], v53 offset:53248
	ds_read_b128 v[196:199], v53 offset:54272
	ds_read_b128 v[200:203], v53 offset:55296
	ds_read_b128 v[204:207], v53 offset:56320
	global_load_lds_dwordx4 v[164:165], off
	v_lshl_add_u64 v[164:165], v[242:243], 0, s[46:47]
	s_mov_b32 m0, s25
	s_nop 0
	global_load_lds_dwordx4 v[164:165], off
	s_barrier
	s_waitcnt lgkmcnt(0)
	s_waitcnt lgkmcnt(0)
	v_mfma_f32_16x16x32_bf16 v[2:5], v[116:119], v[148:151], v[2:5]
	v_mfma_f32_16x16x32_bf16 v[2:5], v[120:123], v[152:155], v[2:5]
	v_mfma_f32_16x16x32_bf16 v[156:159], v[140:143], v[148:151], v[156:159]
	v_mfma_f32_16x16x32_bf16 v[160:163], v[116:119], v[184:187], v[160:163]
	v_mfma_f32_16x16x32_bf16 v[172:175], v[140:143], v[184:187], v[172:175]
	v_mfma_f32_16x16x32_bf16 v[176:179], v[116:119], v[192:195], v[176:179]
	v_mfma_f32_16x16x32_bf16 v[180:183], v[140:143], v[192:195], v[180:183]
	v_mfma_f32_16x16x32_bf16 v[10:13], v[116:119], v[200:203], v[10:13]
	v_mfma_f32_16x16x32_bf16 v[14:17], v[140:143], v[200:203], v[14:17]
	v_mfma_f32_16x16x32_bf16 v[156:159], v[144:147], v[152:155], v[156:159]
	v_mfma_f32_16x16x32_bf16 v[160:163], v[120:123], v[188:191], v[160:163]
	v_mfma_f32_16x16x32_bf16 v[172:175], v[144:147], v[188:191], v[172:175]
	v_mfma_f32_16x16x32_bf16 v[176:179], v[120:123], v[196:199], v[176:179]
	v_mfma_f32_16x16x32_bf16 v[180:183], v[144:147], v[196:199], v[180:183]
	v_mfma_f32_16x16x32_bf16 v[10:13], v[120:123], v[204:207], v[10:13]
	v_mfma_f32_16x16x32_bf16 v[14:17], v[144:147], v[204:207], v[14:17]
	s_barrier
	s_add_u32 s40, s14, 0x18180
	s_addc_u32 s41, s15, 0
	s_add_i32 s15, s33, s19
	v_lshl_add_u64 v[116:117], s[40:41], 0, v[36:37]
	s_mov_b32 m0, s15
	s_add_i32 s14, s15, 0x2000
	global_load_lds_dwordx4 v[116:117], off
	v_lshl_add_u64 v[116:117], s[40:41], 0, v[34:35]
	s_mov_b32 m0, s14
	s_nop 0
	global_load_lds_dwordx4 v[116:117], off
	s_waitcnt vmcnt(6)
	s_barrier
	v_mfma_f32_16x16x32_bf16 v[18:21], v[208:211], v[148:151], v[18:21]
	v_mfma_f32_16x16x32_bf16 v[22:25], v[230:233], v[148:151], v[22:25]
	v_mfma_f32_16x16x32_bf16 v[72:75], v[208:211], v[184:187], v[72:75]
	v_mfma_f32_16x16x32_bf16 v[116:119], v[230:233], v[184:187], v[128:131]
	v_mfma_f32_16x16x32_bf16 v[120:123], v[208:211], v[192:195], v[132:135]
	v_mfma_f32_16x16x32_bf16 v[128:131], v[230:233], v[192:195], v[136:139]
	v_mfma_f32_16x16x32_bf16 v[108:111], v[208:211], v[200:203], v[108:111]
	v_mfma_f32_16x16x32_bf16 v[112:115], v[230:233], v[200:203], v[112:115]
	v_mfma_f32_16x16x32_bf16 v[18:21], v[212:215], v[152:155], v[18:21]
	v_mfma_f32_16x16x32_bf16 v[22:25], v[234:237], v[152:155], v[22:25]
	v_mfma_f32_16x16x32_bf16 v[72:75], v[212:215], v[188:191], v[72:75]
	v_mfma_f32_16x16x32_bf16 v[116:119], v[234:237], v[188:191], v[116:119]
	v_mfma_f32_16x16x32_bf16 v[120:123], v[212:215], v[196:199], v[120:123]
	v_mfma_f32_16x16x32_bf16 v[128:131], v[234:237], v[196:199], v[128:131]
	v_mfma_f32_16x16x32_bf16 v[108:111], v[212:215], v[204:207], v[108:111]
	v_mfma_f32_16x16x32_bf16 v[112:115], v[234:237], v[204:207], v[112:115]
	s_barrier
	ds_read_b128 v[132:135], v39
	ds_read_b128 v[136:139], v39 offset:1024
	ds_read_b128 v[140:143], v39 offset:2048
	ds_read_b128 v[144:147], v39 offset:3072
	s_mov_b32 m0, s35
	v_lshl_add_u64 v[8:9], v[8:9], 0, s[46:47]
	ds_read_b128 v[148:151], v53
	ds_read_b128 v[152:155], v53 offset:1024
	ds_read_b128 v[184:187], v53 offset:2048
	ds_read_b128 v[188:191], v53 offset:3072
	ds_read_b128 v[192:195], v53 offset:4096
	ds_read_b128 v[196:199], v53 offset:5120
	ds_read_b128 v[200:203], v53 offset:6144
	ds_read_b128 v[204:207], v53 offset:7168
	global_load_lds_dwordx4 v[8:9], off
	v_lshl_add_u64 v[6:7], v[6:7], 0, s[46:47]
	s_mov_b32 m0, s8
	s_nop 0
	global_load_lds_dwordx4 v[6:7], off
	s_waitcnt lgkmcnt(8)
	s_barrier
	s_waitcnt lgkmcnt(0)
	s_waitcnt lgkmcnt(0)
	v_mfma_f32_16x16x32_bf16 v[6:9], v[132:135], v[148:151], v[76:79]
	v_mfma_f32_16x16x32_bf16 v[6:9], v[136:139], v[152:155], v[6:9]
	v_mfma_f32_16x16x32_bf16 v[76:79], v[140:143], v[148:151], v[80:83]
	v_mfma_f32_16x16x32_bf16 v[80:83], v[132:135], v[184:187], v[84:87]
	v_mfma_f32_16x16x32_bf16 v[84:87], v[140:143], v[184:187], v[88:91]
	v_mfma_f32_16x16x32_bf16 v[88:91], v[132:135], v[192:195], v[92:95]
	v_mfma_f32_16x16x32_bf16 v[92:95], v[140:143], v[192:195], v[96:99]
	v_mfma_f32_16x16x32_bf16 v[96:99], v[132:135], v[200:203], v[100:103]
	v_mfma_f32_16x16x32_bf16 v[100:103], v[140:143], v[200:203], v[104:107]
	v_mfma_f32_16x16x32_bf16 v[76:79], v[144:147], v[152:155], v[76:79]
	v_mfma_f32_16x16x32_bf16 v[80:83], v[136:139], v[188:191], v[80:83]
	v_mfma_f32_16x16x32_bf16 v[84:87], v[144:147], v[188:191], v[84:87]
	v_mfma_f32_16x16x32_bf16 v[88:91], v[136:139], v[196:199], v[88:91]
	v_mfma_f32_16x16x32_bf16 v[92:95], v[144:147], v[196:199], v[92:95]
	v_mfma_f32_16x16x32_bf16 v[96:99], v[136:139], v[204:207], v[96:99]
	v_mfma_f32_16x16x32_bf16 v[100:103], v[144:147], v[204:207], v[100:103]
	s_barrier
	s_mov_b32 m0, s36
	v_lshl_add_u64 v[164:165], s[6:7], 0, v[36:37]
	ds_read_b128 v[104:107], v41
	ds_read_b128 v[208:211], v41 offset:1024
	ds_read_b128 v[212:215], v41 offset:2048
	ds_read_b128 v[230:233], v41 offset:3072
	global_load_lds_dwordx4 v[164:165], off
	v_lshl_add_u64 v[238:239], s[6:7], 0, v[34:35]
	s_mov_b32 m0, s34
	s_nop 0
	global_load_lds_dwordx4 v[238:239], off
	s_barrier
	s_waitcnt lgkmcnt(0)
	s_waitcnt lgkmcnt(0)
	v_mfma_f32_16x16x32_bf16 v[124:127], v[104:107], v[148:151], v[124:127]
	v_mfma_f32_16x16x32_bf16 v[26:29], v[212:215], v[148:151], v[26:29]
	v_mfma_f32_16x16x32_bf16 v[30:33], v[104:107], v[184:187], v[30:33]
	v_mfma_f32_16x16x32_bf16 v[42:45], v[212:215], v[184:187], v[42:45]
	v_mfma_f32_16x16x32_bf16 v[56:59], v[104:107], v[192:195], v[56:59]
	v_mfma_f32_16x16x32_bf16 v[60:63], v[212:215], v[192:195], v[60:63]
	v_mfma_f32_16x16x32_bf16 v[64:67], v[104:107], v[200:203], v[64:67]
	v_mfma_f32_16x16x32_bf16 v[68:71], v[212:215], v[200:203], v[68:71]
	v_mfma_f32_16x16x32_bf16 v[124:127], v[208:211], v[152:155], v[124:127]
	v_mfma_f32_16x16x32_bf16 v[26:29], v[230:233], v[152:155], v[26:29]
	v_mfma_f32_16x16x32_bf16 v[30:33], v[208:211], v[188:191], v[30:33]
	v_mfma_f32_16x16x32_bf16 v[42:45], v[230:233], v[188:191], v[42:45]
	v_mfma_f32_16x16x32_bf16 v[56:59], v[208:211], v[196:199], v[56:59]
	v_mfma_f32_16x16x32_bf16 v[60:63], v[230:233], v[196:199], v[60:63]
	v_mfma_f32_16x16x32_bf16 v[64:67], v[208:211], v[204:207], v[64:67]
	v_mfma_f32_16x16x32_bf16 v[68:71], v[230:233], v[204:207], v[68:71]
	s_mov_b32 m0, s20
	s_barrier
	ds_read_b128 v[148:151], v53 offset:16384
	ds_read_b128 v[152:155], v53 offset:17408
	ds_read_b128 v[184:187], v53 offset:18432
	ds_read_b128 v[188:191], v53 offset:19456
	ds_read_b128 v[192:195], v53 offset:20480
	ds_read_b128 v[196:199], v53 offset:21504
	ds_read_b128 v[200:203], v53 offset:22528
	ds_read_b128 v[204:207], v53 offset:23552
	global_load_lds_dwordx4 v38, s[12:13]
	s_mov_b32 m0, s21
	v_mov_b32_e32 v39, v227
	global_load_lds_dwordx4 v40, s[12:13]
	s_barrier
	s_waitcnt lgkmcnt(0)
	v_mov_b32_e32 v41, v227
	v_lshl_add_u64 v[246:247], s[12:13], 0, v[38:39]
	v_lshl_add_u64 v[248:249], s[12:13], 0, v[40:41]
	s_waitcnt lgkmcnt(0)
	v_mfma_f32_16x16x32_bf16 v[2:5], v[132:135], v[148:151], v[2:5]
	v_mfma_f32_16x16x32_bf16 v[2:5], v[136:139], v[152:155], v[2:5]
	v_mfma_f32_16x16x32_bf16 v[156:159], v[140:143], v[148:151], v[156:159]
	v_mfma_f32_16x16x32_bf16 v[160:163], v[132:135], v[184:187], v[160:163]
	v_mfma_f32_16x16x32_bf16 v[172:175], v[140:143], v[184:187], v[172:175]
	v_mfma_f32_16x16x32_bf16 v[176:179], v[132:135], v[192:195], v[176:179]
	v_mfma_f32_16x16x32_bf16 v[180:183], v[140:143], v[192:195], v[180:183]
	v_mfma_f32_16x16x32_bf16 v[10:13], v[132:135], v[200:203], v[10:13]
	v_mfma_f32_16x16x32_bf16 v[14:17], v[140:143], v[200:203], v[14:17]
	v_mfma_f32_16x16x32_bf16 v[156:159], v[144:147], v[152:155], v[156:159]
	v_mfma_f32_16x16x32_bf16 v[160:163], v[136:139], v[188:191], v[160:163]
	v_mfma_f32_16x16x32_bf16 v[172:175], v[144:147], v[188:191], v[172:175]
	v_mfma_f32_16x16x32_bf16 v[176:179], v[136:139], v[196:199], v[176:179]
	v_mfma_f32_16x16x32_bf16 v[180:183], v[144:147], v[196:199], v[180:183]
	v_mfma_f32_16x16x32_bf16 v[10:13], v[136:139], v[204:207], v[10:13]
	v_mfma_f32_16x16x32_bf16 v[14:17], v[144:147], v[204:207], v[14:17]
	s_barrier
	s_add_u32 s34, s6, 0x18000
	s_addc_u32 s35, s7, 0
	s_mov_b32 m0, s37
	v_lshl_add_u64 v[132:133], s[34:35], 0, v[36:37]
	global_load_lds_dwordx4 v[132:133], off
	v_lshl_add_u64 v[132:133], s[34:35], 0, v[34:35]
	s_mov_b32 m0, s9
	s_nop 0
	global_load_lds_dwordx4 v[132:133], off
	s_waitcnt vmcnt(6)
	s_barrier
	v_mfma_f32_16x16x32_bf16 v[18:21], v[104:107], v[148:151], v[18:21]
	v_mfma_f32_16x16x32_bf16 v[132:135], v[208:211], v[152:155], v[18:21]
	v_mfma_f32_16x16x32_bf16 v[18:21], v[212:215], v[148:151], v[22:25]
	v_mfma_f32_16x16x32_bf16 v[136:139], v[230:233], v[152:155], v[18:21]
	v_mfma_f32_16x16x32_bf16 v[18:21], v[104:107], v[184:187], v[72:75]
	v_mfma_f32_16x16x32_bf16 v[72:75], v[208:211], v[188:191], v[18:21]
	v_mfma_f32_16x16x32_bf16 v[18:21], v[212:215], v[184:187], v[116:119]
	v_mfma_f32_16x16x32_bf16 v[116:119], v[230:233], v[188:191], v[18:21]
	v_mfma_f32_16x16x32_bf16 v[18:21], v[104:107], v[192:195], v[120:123]
	v_mfma_f32_16x16x32_bf16 v[120:123], v[208:211], v[196:199], v[18:21]
	v_mfma_f32_16x16x32_bf16 v[18:21], v[212:215], v[192:195], v[128:131]
	v_mfma_f32_16x16x32_bf16 v[128:131], v[230:233], v[196:199], v[18:21]
	v_mfma_f32_16x16x32_bf16 v[18:21], v[104:107], v[200:203], v[108:111]
	v_mfma_f32_16x16x32_bf16 v[104:107], v[208:211], v[204:207], v[18:21]
	v_mfma_f32_16x16x32_bf16 v[18:21], v[212:215], v[200:203], v[112:115]
	v_mfma_f32_16x16x32_bf16 v[108:111], v[230:233], v[204:207], v[18:21]
	s_barrier
	ds_read_b128 v[112:115], v166
	ds_read_b128 v[140:143], v166 offset:1024
	ds_read_b128 v[144:147], v166 offset:2048
	ds_read_b128 v[148:151], v166 offset:3072
	s_mov_b32 m0, s22
	ds_read_b128 v[18:21], v53 offset:32768
	ds_read_b128 v[22:25], v53 offset:33792
	ds_read_b128 v[152:155], v53 offset:34816
	ds_read_b128 v[184:187], v53 offset:35840
	ds_read_b128 v[188:191], v53 offset:36864
	ds_read_b128 v[192:195], v53 offset:37888
	ds_read_b128 v[196:199], v53 offset:38912
	ds_read_b128 v[200:203], v53 offset:39936
	global_load_lds_dwordx4 v54, s[12:13]
	s_mov_b32 m0, s23
	s_nop 0
	global_load_lds_dwordx4 v55, s[12:13]
	s_waitcnt lgkmcnt(8)
	s_barrier
	s_waitcnt lgkmcnt(0)
	s_waitcnt lgkmcnt(0)
	v_mfma_f32_16x16x32_bf16 v[6:9], v[112:115], v[18:21], v[6:9]
	v_mfma_f32_16x16x32_bf16 v[204:207], v[140:143], v[22:25], v[6:9]
	v_mfma_f32_16x16x32_bf16 v[6:9], v[144:147], v[18:21], v[76:79]
	v_mfma_f32_16x16x32_bf16 v[76:79], v[148:151], v[22:25], v[6:9]
	v_mfma_f32_16x16x32_bf16 v[6:9], v[112:115], v[152:155], v[80:83]
	v_mfma_f32_16x16x32_bf16 v[80:83], v[140:143], v[184:187], v[6:9]
	v_mfma_f32_16x16x32_bf16 v[6:9], v[144:147], v[152:155], v[84:87]
	v_mfma_f32_16x16x32_bf16 v[84:87], v[148:151], v[184:187], v[6:9]
	v_mfma_f32_16x16x32_bf16 v[6:9], v[112:115], v[188:191], v[88:91]
	v_mfma_f32_16x16x32_bf16 v[88:91], v[140:143], v[192:195], v[6:9]
	v_mfma_f32_16x16x32_bf16 v[6:9], v[144:147], v[188:191], v[92:95]
	v_mfma_f32_16x16x32_bf16 v[92:95], v[148:151], v[192:195], v[6:9]
	v_mfma_f32_16x16x32_bf16 v[6:9], v[112:115], v[196:199], v[96:99]
	v_mfma_f32_16x16x32_bf16 v[96:99], v[140:143], v[200:203], v[6:9]
	v_mfma_f32_16x16x32_bf16 v[6:9], v[144:147], v[196:199], v[100:103]
	v_mfma_f32_16x16x32_bf16 v[100:103], v[148:151], v[200:203], v[6:9]
	s_barrier
	s_mov_b32 m0, s39
	s_nop 3
	v_lshl_add_u64 v[6:7], v[164:165], 0, s[96:97]
	ds_read_b128 v[208:211], v167
	ds_read_b128 v[212:215], v167 offset:1024
	ds_read_b128 v[230:233], v167 offset:2048
	ds_read_b128 v[234:237], v167 offset:3072
	global_load_lds_dwordx4 v[6:7], off
	v_lshl_add_u64 v[6:7], v[238:239], 0, s[96:97]
	s_mov_b32 m0, s38
	s_nop 0
	global_load_lds_dwordx4 v[6:7], off
	s_barrier
	s_waitcnt lgkmcnt(0)
	s_waitcnt lgkmcnt(0)
	v_mfma_f32_16x16x32_bf16 v[6:9], v[208:211], v[18:21], v[124:127]
	v_mfma_f32_16x16x32_bf16 v[124:127], v[212:215], v[22:25], v[6:9]
	v_mfma_f32_16x16x32_bf16 v[6:9], v[230:233], v[18:21], v[26:29]
	v_mfma_f32_16x16x32_bf16 v[238:241], v[234:237], v[22:25], v[6:9]
	v_mfma_f32_16x16x32_bf16 v[6:9], v[208:211], v[152:155], v[30:33]
	v_mfma_f32_16x16x32_bf16 v[242:245], v[212:215], v[184:187], v[6:9]
	v_mfma_f32_16x16x32_bf16 v[6:9], v[230:233], v[152:155], v[42:45]
	v_mfma_f32_16x16x32_bf16 v[152:155], v[234:237], v[184:187], v[6:9]
	v_mfma_f32_16x16x32_bf16 v[6:9], v[208:211], v[188:191], v[56:59]
	v_mfma_f32_16x16x32_bf16 v[56:59], v[212:215], v[192:195], v[6:9]
	v_mfma_f32_16x16x32_bf16 v[6:9], v[230:233], v[188:191], v[60:63]
	v_mfma_f32_16x16x32_bf16 v[60:63], v[234:237], v[192:195], v[6:9]
	v_mfma_f32_16x16x32_bf16 v[6:9], v[208:211], v[196:199], v[64:67]
	v_mfma_f32_16x16x32_bf16 v[64:67], v[212:215], v[200:203], v[6:9]
	v_mfma_f32_16x16x32_bf16 v[6:9], v[230:233], v[196:199], v[68:71]
	v_mfma_f32_16x16x32_bf16 v[68:71], v[234:237], v[200:203], v[6:9]
	s_mov_b32 m0, s24
	s_nop 4
	v_lshl_add_u64 v[6:7], v[246:247], 0, s[96:97]
	s_barrier
	ds_read_b128 v[26:29], v53 offset:49152
	ds_read_b128 v[30:33], v53 offset:50176
	ds_read_b128 v[42:45], v53 offset:51200
	ds_read_b128 v[184:187], v53 offset:52224
	ds_read_b128 v[188:191], v53 offset:53248
	ds_read_b128 v[192:195], v53 offset:54272
	ds_read_b128 v[196:199], v53 offset:55296
	ds_read_b128 v[200:203], v53 offset:56320
	global_load_lds_dwordx4 v[6:7], off
	v_lshl_add_u64 v[6:7], v[248:249], 0, s[96:97]
	s_mov_b32 m0, s25
	s_nop 0
	global_load_lds_dwordx4 v[6:7], off
	s_barrier
	s_waitcnt lgkmcnt(0)
	s_waitcnt lgkmcnt(0)
	v_mfma_f32_16x16x32_bf16 v[2:5], v[112:115], v[26:29], v[2:5]
	v_mfma_f32_16x16x32_bf16 v[246:249], v[140:143], v[30:33], v[2:5]
	v_mfma_f32_16x16x32_bf16 v[2:5], v[144:147], v[26:29], v[156:159]
	v_mfma_f32_16x16x32_bf16 v[156:159], v[148:151], v[30:33], v[2:5]
	v_mfma_f32_16x16x32_bf16 v[2:5], v[112:115], v[42:45], v[160:163]
	v_mfma_f32_16x16x32_bf16 v[160:163], v[140:143], v[184:187], v[2:5]
	v_mfma_f32_16x16x32_bf16 v[2:5], v[144:147], v[42:45], v[172:175]
	v_mfma_f32_16x16x32_bf16 v[172:175], v[148:151], v[184:187], v[2:5]
	v_mfma_f32_16x16x32_bf16 v[2:5], v[112:115], v[188:191], v[176:179]
	v_mfma_f32_16x16x32_bf16 v[22:25], v[140:143], v[192:195], v[2:5]
	v_mfma_f32_16x16x32_bf16 v[2:5], v[144:147], v[188:191], v[180:183]
	v_mfma_f32_16x16x32_bf16 v[18:21], v[148:151], v[192:195], v[2:5]
	v_mfma_f32_16x16x32_bf16 v[2:5], v[112:115], v[196:199], v[10:13]
	v_mfma_f32_16x16x32_bf16 v[6:9], v[140:143], v[200:203], v[2:5]
	v_mfma_f32_16x16x32_bf16 v[2:5], v[144:147], v[196:199], v[14:17]
	v_mfma_f32_16x16x32_bf16 v[2:5], v[148:151], v[200:203], v[2:5]
	s_barrier
	s_add_u32 s8, s6, 0x18080
	s_addc_u32 s9, s7, 0
	s_mov_b32 m0, s15
	v_lshl_add_u64 v[10:11], s[8:9], 0, v[36:37]
	global_load_lds_dwordx4 v[10:11], off
	v_lshl_add_u64 v[10:11], s[8:9], 0, v[34:35]
	s_mov_b32 m0, s14
	s_nop 0
	global_load_lds_dwordx4 v[10:11], off
	s_waitcnt vmcnt(6)
	s_barrier
	v_mfma_f32_16x16x32_bf16 v[10:13], v[208:211], v[26:29], v[132:135]
	v_mfma_f32_16x16x32_bf16 v[112:115], v[212:215], v[30:33], v[10:13]
	v_mfma_f32_16x16x32_bf16 v[10:13], v[230:233], v[26:29], v[136:139]
	v_mfma_f32_16x16x32_bf16 v[132:135], v[234:237], v[30:33], v[10:13]
	v_mfma_f32_16x16x32_bf16 v[10:13], v[208:211], v[42:45], v[72:75]
	v_mfma_f32_16x16x32_bf16 v[72:75], v[212:215], v[184:187], v[10:13]
	v_mfma_f32_16x16x32_bf16 v[10:13], v[230:233], v[42:45], v[116:119]
	v_mfma_f32_16x16x32_bf16 v[116:119], v[234:237], v[184:187], v[10:13]
	v_mfma_f32_16x16x32_bf16 v[10:13], v[208:211], v[188:191], v[120:123]
	v_mfma_f32_16x16x32_bf16 v[30:33], v[212:215], v[192:195], v[10:13]
	v_mfma_f32_16x16x32_bf16 v[10:13], v[230:233], v[188:191], v[128:131]
	v_mfma_f32_16x16x32_bf16 v[26:29], v[234:237], v[192:195], v[10:13]
	v_mfma_f32_16x16x32_bf16 v[10:13], v[208:211], v[196:199], v[104:107]
	v_mfma_f32_16x16x32_bf16 v[14:17], v[212:215], v[200:203], v[10:13]
	v_mfma_f32_16x16x32_bf16 v[10:13], v[230:233], v[196:199], v[108:111]
	v_mfma_f32_16x16x32_bf16 v[10:13], v[234:237], v[200:203], v[10:13]
	v_lshl_or_b32 v44, s31, 8, v52
	v_lshl_add_u32 v39, s30, 8, v50
	v_ashrrev_i32_e32 v45, 31, v44
	v_mov_b64_e32 v[42:43], s[10:11]
	v_mad_i64_i32 v[104:105], s[8:9], v39, s59, v[42:43]
	v_lshlrev_b64 v[44:45], 1, v[44:45]
	v_lshl_add_u64 v[108:109], v[104:105], 0, v[44:45]
	s_barrier
	v_cvt_pk_bf16_f32 v104, v204, v205
	v_cvt_pk_bf16_f32 v105, v206, v207
	v_cvt_pk_bf16_f32 v106, v76, v77
	v_cvt_pk_bf16_f32 v107, v78, v79
	global_store_dwordx4 v[108:109], v[104:107], off
	v_cvt_pk_bf16_f32 v76, v124, v125
	v_cvt_pk_bf16_f32 v77, v126, v127
	v_or_b32_e32 v41, 16, v39
	v_cvt_pk_bf16_f32 v78, v238, v239
	v_cvt_pk_bf16_f32 v79, v240, v241
	global_store_dwordx4 v[108:109], v[76:79], off offset:256
	s_add_i32 s27, s27, s79
	s_andn2_b64 vcc, exec, s[4:5]
	v_mad_i64_i32 v[76:77], s[8:9], v41, s59, v[42:43]
	v_lshl_add_u64 v[104:105], v[76:77], 0, v[44:45]
	v_cvt_pk_bf16_f32 v76, v80, v81
	v_cvt_pk_bf16_f32 v77, v82, v83
	v_cvt_pk_bf16_f32 v78, v84, v85
	v_cvt_pk_bf16_f32 v79, v86, v87
	global_store_dwordx4 v[104:105], v[76:79], off
	v_or_b32_e32 v41, 32, v39
	v_mov_b32_e32 v226, v54
	v_cvt_pk_bf16_f32 v76, v242, v243
	v_cvt_pk_bf16_f32 v77, v244, v245
	v_cvt_pk_bf16_f32 v78, v152, v153
	v_cvt_pk_bf16_f32 v79, v154, v155
	global_store_dwordx4 v[104:105], v[76:79], off offset:256
	s_mov_b32 s31, s28
	s_mov_b32 s30, s29
	v_mad_i64_i32 v[76:77], s[8:9], v41, s59, v[42:43]
	v_lshl_add_u64 v[80:81], v[76:77], 0, v[44:45]
	v_cvt_pk_bf16_f32 v76, v88, v89
	v_cvt_pk_bf16_f32 v77, v90, v91
	v_cvt_pk_bf16_f32 v78, v92, v93
	v_cvt_pk_bf16_f32 v79, v94, v95
	global_store_dwordx4 v[80:81], v[76:79], off
	v_cvt_pk_bf16_f32 v56, v56, v57
	v_cvt_pk_bf16_f32 v57, v58, v59
	v_or_b32_e32 v41, 48, v39
	v_cvt_pk_bf16_f32 v58, v60, v61
	v_cvt_pk_bf16_f32 v59, v62, v63
	global_store_dwordx4 v[80:81], v[56:59], off offset:256
	s_mov_b64 s[14:15], s[6:7]
	s_nop 0
	v_mad_i64_i32 v[56:57], s[8:9], v41, s59, v[42:43]
	v_lshl_add_u64 v[60:61], v[56:57], 0, v[44:45]
	v_cvt_pk_bf16_f32 v56, v96, v97
	v_cvt_pk_bf16_f32 v57, v98, v99
	v_cvt_pk_bf16_f32 v58, v100, v101
	v_cvt_pk_bf16_f32 v59, v102, v103
	global_store_dwordx4 v[60:61], v[56:59], off
	v_add_u32_e32 v41, 0x80, v39
	s_nop 0
	v_cvt_pk_bf16_f32 v56, v64, v65
	v_cvt_pk_bf16_f32 v57, v66, v67
	v_cvt_pk_bf16_f32 v58, v68, v69
	v_cvt_pk_bf16_f32 v59, v70, v71
	global_store_dwordx4 v[60:61], v[56:59], off offset:256
	s_nop 1
	v_mad_i64_i32 v[56:57], s[8:9], v41, s59, v[42:43]
	v_lshl_add_u64 v[60:61], v[56:57], 0, v[44:45]
	v_cvt_pk_bf16_f32 v56, v246, v247
	v_cvt_pk_bf16_f32 v57, v248, v249
	v_cvt_pk_bf16_f32 v58, v156, v157
	v_cvt_pk_bf16_f32 v59, v158, v159
	global_store_dwordx4 v[60:61], v[56:59], off
	v_add_u32_e32 v41, 0x90, v39
	s_nop 0
	v_cvt_pk_bf16_f32 v56, v112, v113
	v_cvt_pk_bf16_f32 v57, v114, v115
	v_cvt_pk_bf16_f32 v58, v132, v133
	v_cvt_pk_bf16_f32 v59, v134, v135
	global_store_dwordx4 v[60:61], v[56:59], off offset:256
	s_nop 1
	v_mad_i64_i32 v[56:57], s[8:9], v41, s59, v[42:43]
	v_lshl_add_u64 v[60:61], v[56:57], 0, v[44:45]
	v_cvt_pk_bf16_f32 v56, v160, v161
	v_cvt_pk_bf16_f32 v57, v162, v163
	v_cvt_pk_bf16_f32 v58, v172, v173
	v_cvt_pk_bf16_f32 v59, v174, v175
	global_store_dwordx4 v[60:61], v[56:59], off
	v_add_u32_e32 v41, 0xa0, v39
	s_nop 0
	v_cvt_pk_bf16_f32 v56, v72, v73
	v_cvt_pk_bf16_f32 v57, v74, v75
	v_cvt_pk_bf16_f32 v58, v116, v117
	v_cvt_pk_bf16_f32 v59, v118, v119
	global_store_dwordx4 v[60:61], v[56:59], off offset:256
	v_cvt_pk_bf16_f32 v22, v22, v23
	v_cvt_pk_bf16_f32 v23, v24, v25
	v_cvt_pk_bf16_f32 v24, v18, v19
	v_cvt_pk_bf16_f32 v25, v20, v21
	s_nop 1
	v_mad_i64_i32 v[56:57], s[8:9], v41, s59, v[42:43]
	v_lshl_add_u64 v[56:57], v[56:57], 0, v[44:45]
	global_store_dwordx4 v[56:57], v[22:25], off
	v_cvt_pk_bf16_f32 v18, v30, v31
	v_cvt_pk_bf16_f32 v19, v32, v33
	v_cvt_pk_bf16_f32 v20, v26, v27
	v_cvt_pk_bf16_f32 v21, v28, v29
	global_store_dwordx4 v[56:57], v[18:21], off offset:256
	v_cvt_pk_bf16_f32 v6, v6, v7
	v_cvt_pk_bf16_f32 v7, v8, v9
	v_cvt_pk_bf16_f32 v8, v2, v3
	v_cvt_pk_bf16_f32 v9, v4, v5
	s_nop 1
	v_add_u32_e32 v18, 0xb0, v39
	v_mad_i64_i32 v[18:19], s[8:9], v18, s59, v[42:43]
	v_lshl_add_u64 v[18:19], v[18:19], 0, v[44:45]
	global_store_dwordx4 v[18:19], v[6:9], off
	v_cvt_pk_bf16_f32 v2, v14, v15
	v_cvt_pk_bf16_f32 v3, v16, v17
	v_cvt_pk_bf16_f32 v4, v10, v11
	v_cvt_pk_bf16_f32 v5, v12, v13
	global_store_dwordx4 v[18:19], v[2:5], off offset:256
	s_nop 0
	v_mov_b32_e32 v6, v55
	v_mov_b32_e32 v2, v40
	v_mov_b32_e32 v4, v38
	s_cbranch_vccz .LBB0_436

.LBB0_989:
	s_add_u32 s20, s8, s0
	s_addc_u32 s21, s9, s1
	s_add_u32 s22, s20, 0x100
	s_addc_u32 s23, s21, 0
	s_add_u32 s33, s50, s0
	s_addc_u32 s57, s51, s1
	s_cmpk_eq_i32 s0, 0x700
	s_cselect_b64 s[58:59], -1, 0
	s_and_b64 s[20:21], s[58:59], exec
	s_cselect_b32 s23, s9, s23
	s_cselect_b32 s22, s8, s22
	s_cselect_b32 s21, s17, s57
	s_cselect_b32 s20, s49, s33
	s_add_i32 s33, 0, 0x10000
	v_add_u32_e32 v123, s33, v201
	ds_read_b128 v[134:137], v123
	ds_read_b128 v[146:149], v123 offset:1024
	ds_read_b128 v[150:153], v123 offset:2048
	ds_read_b128 v[154:157], v123 offset:3072
	s_and_b64 vcc, s[6:7], s[58:59]
	v_cndmask_b32_e32 v226, v122, v204, vcc
	v_cndmask_b32_e32 v166, v124, v205, vcc
	v_cndmask_b32_e32 v123, v128, v206, vcc
	v_cndmask_b32_e32 v125, v126, v207, vcc
	v_lshl_add_u64 v[238:239], v[132:133], 0, s[0:1]
	s_add_i32 m0, s36, 0xc000
	ds_read_b128 v[158:161], v203
	ds_read_b128 v[162:165], v203 offset:1024
	ds_read_b128 v[192:195], v203 offset:2048
	ds_read_b128 v[196:199], v203 offset:3072
	ds_read_b128 v[208:211], v203 offset:4096
	ds_read_b128 v[212:215], v203 offset:5120
	ds_read_b128 v[230:233], v203 offset:6144
	ds_read_b128 v[234:237], v203 offset:7168
	global_load_lds_dwordx4 v[238:239], off
	v_lshl_add_u64 v[238:239], v[130:131], 0, s[0:1]
	s_add_i32 m0, s36, 0xe000
	s_nop 0
	global_load_lds_dwordx4 v[238:239], off
	s_waitcnt lgkmcnt(8)
	s_barrier
	s_waitcnt lgkmcnt(0)
	s_waitcnt lgkmcnt(0)
	v_mfma_f32_16x16x32_bf16 v[142:145], v[134:137], v[158:161], v[142:145]
	v_mfma_f32_16x16x32_bf16 v[138:141], v[150:153], v[158:161], v[138:141]
	v_mfma_f32_16x16x32_bf16 v[110:113], v[134:137], v[192:195], v[110:113]
	v_mfma_f32_16x16x32_bf16 v[106:109], v[150:153], v[192:195], v[106:109]
	v_mfma_f32_16x16x32_bf16 v[94:97], v[134:137], v[208:211], v[94:97]
	v_mfma_f32_16x16x32_bf16 v[90:93], v[150:153], v[208:211], v[90:93]
	v_mfma_f32_16x16x32_bf16 v[78:81], v[134:137], v[230:233], v[78:81]
	v_mfma_f32_16x16x32_bf16 v[74:77], v[150:153], v[230:233], v[74:77]
	v_mfma_f32_16x16x32_bf16 v[142:145], v[146:149], v[162:165], v[142:145]
	v_mfma_f32_16x16x32_bf16 v[138:141], v[154:157], v[162:165], v[138:141]
	v_mfma_f32_16x16x32_bf16 v[110:113], v[146:149], v[196:199], v[110:113]
	v_mfma_f32_16x16x32_bf16 v[106:109], v[154:157], v[196:199], v[106:109]
	v_mfma_f32_16x16x32_bf16 v[94:97], v[146:149], v[212:215], v[94:97]
	v_mfma_f32_16x16x32_bf16 v[90:93], v[154:157], v[212:215], v[90:93]
	v_mfma_f32_16x16x32_bf16 v[78:81], v[146:149], v[234:237], v[78:81]
	v_mfma_f32_16x16x32_bf16 v[74:77], v[154:157], v[234:237], v[74:77]
	s_barrier
	s_add_i32 s57, 0, 0x14000
	s_add_i32 s33, s33, s28
	v_add_u32_e32 v127, s57, v201
	v_lshl_add_u64 v[222:223], s[20:21], 0, v[174:175]
	s_mov_b32 m0, s33
	ds_read_b128 v[238:241], v127
	ds_read_b128 v[242:245], v127 offset:1024
	ds_read_b128 v[246:249], v127 offset:2048
	ds_read_b128 v[250:253], v127 offset:3072
	global_load_lds_dwordx4 v[222:223], off
	v_lshl_add_u64 v[224:225], s[20:21], 0, v[172:173]
	s_add_i32 m0, s33, 0x2000
	s_nop 0
	global_load_lds_dwordx4 v[224:225], off
	s_barrier
	s_waitcnt lgkmcnt(0)
	s_waitcnt lgkmcnt(0)
	v_mfma_f32_16x16x32_bf16 v[118:121], v[238:241], v[158:161], v[118:121]
	v_mfma_f32_16x16x32_bf16 v[114:117], v[246:249], v[158:161], v[114:117]
	v_mfma_f32_16x16x32_bf16 v[102:105], v[238:241], v[192:195], v[102:105]
	v_mfma_f32_16x16x32_bf16 v[98:101], v[246:249], v[192:195], v[98:101]
	v_mfma_f32_16x16x32_bf16 v[86:89], v[238:241], v[208:211], v[86:89]
	v_mfma_f32_16x16x32_bf16 v[82:85], v[246:249], v[208:211], v[82:85]
	v_mfma_f32_16x16x32_bf16 v[70:73], v[238:241], v[230:233], v[70:73]
	v_mfma_f32_16x16x32_bf16 v[66:69], v[246:249], v[230:233], v[66:69]
	v_mfma_f32_16x16x32_bf16 v[118:121], v[242:245], v[162:165], v[118:121]
	v_mfma_f32_16x16x32_bf16 v[114:117], v[250:253], v[162:165], v[114:117]
	v_mfma_f32_16x16x32_bf16 v[102:105], v[242:245], v[196:199], v[102:105]
	v_mfma_f32_16x16x32_bf16 v[98:101], v[250:253], v[196:199], v[98:101]
	v_mfma_f32_16x16x32_bf16 v[86:89], v[242:245], v[212:215], v[86:89]
	v_mfma_f32_16x16x32_bf16 v[82:85], v[250:253], v[212:215], v[82:85]
	v_mfma_f32_16x16x32_bf16 v[70:73], v[242:245], v[234:237], v[70:73]
	v_mfma_f32_16x16x32_bf16 v[66:69], v[250:253], v[234:237], v[66:69]
	s_mov_b32 m0, s36
	s_barrier
	ds_read_b128 v[158:161], v203 offset:16384
	ds_read_b128 v[162:165], v203 offset:17408
	ds_read_b128 v[192:195], v203 offset:18432
	ds_read_b128 v[196:199], v203 offset:19456
	ds_read_b128 v[208:211], v203 offset:20480
	ds_read_b128 v[212:215], v203 offset:21504
	ds_read_b128 v[230:233], v203 offset:22528
	ds_read_b128 v[234:237], v203 offset:23552
	global_load_lds_dwordx4 v226, s[22:23]
	s_mov_b32 m0, s37
	v_mov_b32_e32 v167, v227
	global_load_lds_dwordx4 v166, s[22:23]
	s_barrier
	s_waitcnt lgkmcnt(0)
	v_lshl_add_u64 v[220:221], s[22:23], 0, v[226:227]
	v_lshl_add_u64 v[166:167], s[22:23], 0, v[166:167]
	s_waitcnt lgkmcnt(0)
	v_mfma_f32_16x16x32_bf16 v[54:57], v[134:137], v[158:161], v[54:57]
	v_mfma_f32_16x16x32_bf16 v[50:53], v[150:153], v[158:161], v[50:53]
	v_mfma_f32_16x16x32_bf16 v[38:41], v[134:137], v[192:195], v[38:41]
	v_mfma_f32_16x16x32_bf16 v[34:37], v[150:153], v[192:195], v[34:37]
	v_mfma_f32_16x16x32_bf16 v[22:25], v[134:137], v[208:211], v[22:25]
	v_mfma_f32_16x16x32_bf16 v[18:21], v[150:153], v[208:211], v[18:21]
	v_mfma_f32_16x16x32_bf16 v[6:9], v[134:137], v[230:233], v[6:9]
	v_mfma_f32_16x16x32_bf16 v[2:5], v[150:153], v[230:233], v[2:5]
	v_mfma_f32_16x16x32_bf16 v[54:57], v[146:149], v[162:165], v[54:57]
	v_mfma_f32_16x16x32_bf16 v[50:53], v[154:157], v[162:165], v[50:53]
	v_mfma_f32_16x16x32_bf16 v[38:41], v[146:149], v[196:199], v[38:41]
	v_mfma_f32_16x16x32_bf16 v[34:37], v[154:157], v[196:199], v[34:37]
	v_mfma_f32_16x16x32_bf16 v[22:25], v[146:149], v[212:215], v[22:25]
	v_mfma_f32_16x16x32_bf16 v[18:21], v[154:157], v[212:215], v[18:21]
	v_mfma_f32_16x16x32_bf16 v[6:9], v[146:149], v[234:237], v[6:9]
	v_mfma_f32_16x16x32_bf16 v[2:5], v[154:157], v[234:237], v[2:5]
	s_barrier
	s_add_u32 s58, s20, 0x40000
	s_addc_u32 s59, s21, 0
	s_add_i32 s33, s57, s28
	v_lshl_add_u64 v[134:135], s[58:59], 0, v[174:175]
	s_mov_b32 m0, s33
	s_nop 0
	global_load_lds_dwordx4 v[134:135], off
	v_lshl_add_u64 v[134:135], s[58:59], 0, v[172:173]
	s_add_i32 m0, s33, 0x2000
	s_nop 0
	global_load_lds_dwordx4 v[134:135], off
	s_waitcnt vmcnt(6)
	s_barrier
	v_mfma_f32_16x16x32_bf16 v[62:65], v[238:241], v[158:161], v[62:65]
	v_mfma_f32_16x16x32_bf16 v[58:61], v[246:249], v[158:161], v[58:61]
	v_mfma_f32_16x16x32_bf16 v[46:49], v[238:241], v[192:195], v[46:49]
	v_mfma_f32_16x16x32_bf16 v[42:45], v[246:249], v[192:195], v[42:45]
	v_mfma_f32_16x16x32_bf16 v[30:33], v[238:241], v[208:211], v[30:33]
	v_mfma_f32_16x16x32_bf16 v[26:29], v[246:249], v[208:211], v[26:29]
	v_mfma_f32_16x16x32_bf16 v[14:17], v[238:241], v[230:233], v[14:17]
	v_mfma_f32_16x16x32_bf16 v[10:13], v[246:249], v[230:233], v[10:13]
	v_mfma_f32_16x16x32_bf16 v[62:65], v[242:245], v[162:165], v[62:65]
	v_mfma_f32_16x16x32_bf16 v[58:61], v[250:253], v[162:165], v[58:61]
	v_mfma_f32_16x16x32_bf16 v[46:49], v[242:245], v[196:199], v[46:49]
	v_mfma_f32_16x16x32_bf16 v[42:45], v[250:253], v[196:199], v[42:45]
	v_mfma_f32_16x16x32_bf16 v[30:33], v[242:245], v[212:215], v[30:33]
	v_mfma_f32_16x16x32_bf16 v[26:29], v[250:253], v[212:215], v[26:29]
	v_mfma_f32_16x16x32_bf16 v[14:17], v[242:245], v[234:237], v[14:17]
	v_mfma_f32_16x16x32_bf16 v[10:13], v[250:253], v[234:237], v[10:13]
	s_add_i32 s33, 0, 0x18000
	v_add_u32_e32 v127, s33, v201
	s_barrier
	ds_read_b128 v[134:137], v127
	ds_read_b128 v[146:149], v127 offset:1024
	ds_read_b128 v[150:153], v127 offset:2048
	ds_read_b128 v[154:157], v127 offset:3072
	s_mov_b32 m0, s38
	ds_read_b128 v[158:161], v203 offset:32768
	ds_read_b128 v[162:165], v203 offset:33792
	ds_read_b128 v[192:195], v203 offset:34816
	ds_read_b128 v[196:199], v203 offset:35840
	ds_read_b128 v[208:211], v203 offset:36864
	ds_read_b128 v[212:215], v203 offset:37888
	ds_read_b128 v[230:233], v203 offset:38912
	ds_read_b128 v[234:237], v203 offset:39936
	global_load_lds_dwordx4 v123, s[22:23]
	s_mov_b32 m0, s39
	s_nop 0
	global_load_lds_dwordx4 v125, s[22:23]
	s_waitcnt lgkmcnt(8)
	s_barrier
	s_waitcnt lgkmcnt(0)
	s_waitcnt lgkmcnt(0)
	v_mfma_f32_16x16x32_bf16 v[142:145], v[134:137], v[158:161], v[142:145]
	v_mfma_f32_16x16x32_bf16 v[138:141], v[150:153], v[158:161], v[138:141]
	v_mfma_f32_16x16x32_bf16 v[110:113], v[134:137], v[192:195], v[110:113]
	v_mfma_f32_16x16x32_bf16 v[106:109], v[150:153], v[192:195], v[106:109]
	v_mfma_f32_16x16x32_bf16 v[94:97], v[134:137], v[208:211], v[94:97]
	v_mfma_f32_16x16x32_bf16 v[90:93], v[150:153], v[208:211], v[90:93]
	v_mfma_f32_16x16x32_bf16 v[78:81], v[134:137], v[230:233], v[78:81]
	v_mfma_f32_16x16x32_bf16 v[74:77], v[150:153], v[230:233], v[74:77]
	v_mfma_f32_16x16x32_bf16 v[142:145], v[146:149], v[162:165], v[142:145]
	v_mfma_f32_16x16x32_bf16 v[138:141], v[154:157], v[162:165], v[138:141]
	v_mfma_f32_16x16x32_bf16 v[110:113], v[146:149], v[196:199], v[110:113]
	v_mfma_f32_16x16x32_bf16 v[106:109], v[154:157], v[196:199], v[106:109]
	v_mfma_f32_16x16x32_bf16 v[94:97], v[146:149], v[212:215], v[94:97]
	v_mfma_f32_16x16x32_bf16 v[90:93], v[154:157], v[212:215], v[90:93]
	v_mfma_f32_16x16x32_bf16 v[78:81], v[146:149], v[234:237], v[78:81]
	v_mfma_f32_16x16x32_bf16 v[74:77], v[154:157], v[234:237], v[74:77]
	s_barrier
	s_add_i32 s22, 0, 0x1c000
	s_add_i32 s23, s33, s28
	v_add_u32_e32 v123, s22, v201
	v_lshl_add_u64 v[222:223], v[222:223], 0, s[96:97]
	s_mov_b32 m0, s23
	ds_read_b128 v[238:241], v123
	ds_read_b128 v[242:245], v123 offset:1024
	ds_read_b128 v[246:249], v123 offset:2048
	ds_read_b128 v[250:253], v123 offset:3072
	global_load_lds_dwordx4 v[222:223], off
	v_lshl_add_u64 v[222:223], v[224:225], 0, s[96:97]
	s_add_i32 m0, s23, 0x2000
	s_nop 0
	global_load_lds_dwordx4 v[222:223], off
	s_barrier
	s_waitcnt lgkmcnt(0)
	s_waitcnt lgkmcnt(0)
	v_mfma_f32_16x16x32_bf16 v[118:121], v[238:241], v[158:161], v[118:121]
	v_mfma_f32_16x16x32_bf16 v[114:117], v[246:249], v[158:161], v[114:117]
	v_mfma_f32_16x16x32_bf16 v[102:105], v[238:241], v[192:195], v[102:105]
	v_mfma_f32_16x16x32_bf16 v[98:101], v[246:249], v[192:195], v[98:101]
	v_mfma_f32_16x16x32_bf16 v[86:89], v[238:241], v[208:211], v[86:89]
	v_mfma_f32_16x16x32_bf16 v[82:85], v[246:249], v[208:211], v[82:85]
	v_mfma_f32_16x16x32_bf16 v[70:73], v[238:241], v[230:233], v[70:73]
	v_mfma_f32_16x16x32_bf16 v[66:69], v[246:249], v[230:233], v[66:69]
	v_mfma_f32_16x16x32_bf16 v[118:121], v[242:245], v[162:165], v[118:121]
	v_mfma_f32_16x16x32_bf16 v[114:117], v[250:253], v[162:165], v[114:117]
	v_mfma_f32_16x16x32_bf16 v[102:105], v[242:245], v[196:199], v[102:105]
	v_mfma_f32_16x16x32_bf16 v[98:101], v[250:253], v[196:199], v[98:101]
	v_mfma_f32_16x16x32_bf16 v[86:89], v[242:245], v[212:215], v[86:89]
	v_mfma_f32_16x16x32_bf16 v[82:85], v[250:253], v[212:215], v[82:85]
	v_mfma_f32_16x16x32_bf16 v[70:73], v[242:245], v[234:237], v[70:73]
	v_mfma_f32_16x16x32_bf16 v[66:69], v[250:253], v[234:237], v[66:69]
	s_mov_b32 m0, s42
	v_lshl_add_u64 v[220:221], v[220:221], 0, s[96:97]
	s_barrier
	ds_read_b128 v[158:161], v203 offset:49152
	ds_read_b128 v[162:165], v203 offset:50176
	ds_read_b128 v[192:195], v203 offset:51200
	ds_read_b128 v[196:199], v203 offset:52224
	ds_read_b128 v[208:211], v203 offset:53248
	ds_read_b128 v[212:215], v203 offset:54272
	ds_read_b128 v[230:233], v203 offset:55296
	ds_read_b128 v[234:237], v203 offset:56320
	global_load_lds_dwordx4 v[220:221], off
	v_lshl_add_u64 v[166:167], v[166:167], 0, s[96:97]
	s_mov_b32 m0, s43
	s_nop 0
	global_load_lds_dwordx4 v[166:167], off
	s_barrier
	s_waitcnt lgkmcnt(0)
	s_waitcnt lgkmcnt(0)
	v_mfma_f32_16x16x32_bf16 v[54:57], v[134:137], v[158:161], v[54:57]
	v_mfma_f32_16x16x32_bf16 v[50:53], v[150:153], v[158:161], v[50:53]
	v_mfma_f32_16x16x32_bf16 v[38:41], v[134:137], v[192:195], v[38:41]
	v_mfma_f32_16x16x32_bf16 v[34:37], v[150:153], v[192:195], v[34:37]
	v_mfma_f32_16x16x32_bf16 v[22:25], v[134:137], v[208:211], v[22:25]
	v_mfma_f32_16x16x32_bf16 v[18:21], v[150:153], v[208:211], v[18:21]
	v_mfma_f32_16x16x32_bf16 v[6:9], v[134:137], v[230:233], v[6:9]
	v_mfma_f32_16x16x32_bf16 v[2:5], v[150:153], v[230:233], v[2:5]
	v_mfma_f32_16x16x32_bf16 v[54:57], v[146:149], v[162:165], v[54:57]
	v_mfma_f32_16x16x32_bf16 v[50:53], v[154:157], v[162:165], v[50:53]
	v_mfma_f32_16x16x32_bf16 v[38:41], v[146:149], v[196:199], v[38:41]
	v_mfma_f32_16x16x32_bf16 v[34:37], v[154:157], v[196:199], v[34:37]
	v_mfma_f32_16x16x32_bf16 v[22:25], v[146:149], v[212:215], v[22:25]
	v_mfma_f32_16x16x32_bf16 v[18:21], v[154:157], v[212:215], v[18:21]
	v_mfma_f32_16x16x32_bf16 v[6:9], v[146:149], v[234:237], v[6:9]
	v_mfma_f32_16x16x32_bf16 v[2:5], v[154:157], v[234:237], v[2:5]
	s_barrier
	s_add_u32 s20, s20, 0x40080
	s_addc_u32 s21, s21, 0
	s_add_i32 s22, s22, s28
	v_lshl_add_u64 v[134:135], s[20:21], 0, v[174:175]
	s_mov_b32 m0, s22
	s_nop 0
	global_load_lds_dwordx4 v[134:135], off
	v_lshl_add_u64 v[134:135], s[20:21], 0, v[172:173]
	s_add_i32 m0, s22, 0x2000
	s_nop 0
	global_load_lds_dwordx4 v[134:135], off
	s_waitcnt vmcnt(6)
	s_barrier
	v_mfma_f32_16x16x32_bf16 v[62:65], v[238:241], v[158:161], v[62:65]
	v_mfma_f32_16x16x32_bf16 v[58:61], v[246:249], v[158:161], v[58:61]
	v_mfma_f32_16x16x32_bf16 v[46:49], v[238:241], v[192:195], v[46:49]
	v_mfma_f32_16x16x32_bf16 v[42:45], v[246:249], v[192:195], v[42:45]
	v_mfma_f32_16x16x32_bf16 v[30:33], v[238:241], v[208:211], v[30:33]
	v_mfma_f32_16x16x32_bf16 v[26:29], v[246:249], v[208:211], v[26:29]
	v_mfma_f32_16x16x32_bf16 v[14:17], v[238:241], v[230:233], v[14:17]
	v_mfma_f32_16x16x32_bf16 v[10:13], v[246:249], v[230:233], v[10:13]
	v_mfma_f32_16x16x32_bf16 v[62:65], v[242:245], v[162:165], v[62:65]
	v_mfma_f32_16x16x32_bf16 v[58:61], v[250:253], v[162:165], v[58:61]
	v_mfma_f32_16x16x32_bf16 v[46:49], v[242:245], v[196:199], v[46:49]
	v_mfma_f32_16x16x32_bf16 v[42:45], v[250:253], v[196:199], v[42:45]
	v_mfma_f32_16x16x32_bf16 v[30:33], v[242:245], v[212:215], v[30:33]
	v_mfma_f32_16x16x32_bf16 v[26:29], v[250:253], v[212:215], v[26:29]
	v_mfma_f32_16x16x32_bf16 v[14:17], v[242:245], v[234:237], v[14:17]
	v_mfma_f32_16x16x32_bf16 v[10:13], v[250:253], v[234:237], v[10:13]
	s_add_i32 s52, s52, 2
	s_add_u32 s0, s0, 0x100
	s_addc_u32 s1, s1, 0
	s_cmp_gt_u32 s52, 13
	s_barrier
	s_cbranch_scc0 .LBB0_989
	s_cmpk_gt_i32 s47, 0x7f
	s_mov_b64 s[0:1], 0xc000
	s_mov_b32 s49, 0x8000
	s_cbranch_scc1 .LBB0_985
	s_ashr_i32 s0, s47, 31
	s_lshr_b32 s0, s0, 28
	s_add_i32 s0, s47, s0
	s_ashr_i32 s0, s0, 4
	s_mul_i32 s0, s0, 6
	s_ashr_i32 s1, s0, 31
	s_lshl_b64 s[0:1], s[0:1], 10
	s_branch .LBB0_985

.LBB0_1246:
	s_add_u32 s6, s10, s0
	s_addc_u32 s7, s11, s1
	s_add_u32 s24, s6, 0x100
	s_addc_u32 s25, s7, 0
	s_add_u32 s33, s23, s0
	s_addc_u32 s46, s44, s1
	s_cmpk_eq_i32 s0, 0x700
	s_cselect_b64 vcc, -1, 0
	s_and_b64 s[6:7], vcc, exec
	s_cselect_b32 s25, s11, s25
	s_cselect_b32 s24, s10, s24
	s_cselect_b32 s7, s9, s46
	s_cselect_b32 s6, s8, s33
	s_add_i32 s33, 0, 0x10000
	v_add_u32_e32 v165, s33, v141
	ds_read_b128 v[156:159], v165
	ds_read_b128 v[160:163], v165 offset:1024
	ds_read_b128 v[172:175], v165 offset:2048
	ds_read_b128 v[176:179], v165 offset:3072
	v_cndmask_b32_e32 v226, v140, v152, vcc
	v_cndmask_b32_e32 v164, v138, v153, vcc
	v_cndmask_b32_e32 v135, v136, v154, vcc
	v_cndmask_b32_e32 v137, v134, v155, vcc
	v_lshl_add_u64 v[166:167], v[144:145], 0, s[0:1]
	s_add_i32 m0, s31, 0xc000
	ds_read_b128 v[180:183], v151
	ds_read_b128 v[184:187], v151 offset:1024
	ds_read_b128 v[188:191], v151 offset:2048
	ds_read_b128 v[192:195], v151 offset:3072
	ds_read_b128 v[196:199], v151 offset:4096
	ds_read_b128 v[200:203], v151 offset:5120
	ds_read_b128 v[204:207], v151 offset:6144
	ds_read_b128 v[208:211], v151 offset:7168
	global_load_lds_dwordx4 v[166:167], off
	v_lshl_add_u64 v[166:167], v[142:143], 0, s[0:1]
	s_add_i32 m0, s31, 0xe000
	s_nop 0
	global_load_lds_dwordx4 v[166:167], off
	s_waitcnt lgkmcnt(8)
	s_barrier
	s_waitcnt lgkmcnt(0)
	s_waitcnt lgkmcnt(0)
	v_mfma_f32_16x16x32_bf16 v[126:129], v[156:159], v[180:183], v[126:129]
	v_mfma_f32_16x16x32_bf16 v[118:121], v[172:175], v[180:183], v[118:121]
	v_mfma_f32_16x16x32_bf16 v[110:113], v[156:159], v[188:191], v[110:113]
	v_mfma_f32_16x16x32_bf16 v[102:105], v[172:175], v[188:191], v[102:105]
	v_mfma_f32_16x16x32_bf16 v[94:97], v[156:159], v[196:199], v[94:97]
	v_mfma_f32_16x16x32_bf16 v[86:89], v[172:175], v[196:199], v[86:89]
	v_mfma_f32_16x16x32_bf16 v[78:81], v[156:159], v[204:207], v[78:81]
	v_mfma_f32_16x16x32_bf16 v[70:73], v[172:175], v[204:207], v[70:73]
	v_mfma_f32_16x16x32_bf16 v[126:129], v[160:163], v[184:187], v[126:129]
	v_mfma_f32_16x16x32_bf16 v[118:121], v[176:179], v[184:187], v[118:121]
	v_mfma_f32_16x16x32_bf16 v[110:113], v[160:163], v[192:195], v[110:113]
	v_mfma_f32_16x16x32_bf16 v[102:105], v[176:179], v[192:195], v[102:105]
	v_mfma_f32_16x16x32_bf16 v[94:97], v[160:163], v[200:203], v[94:97]
	v_mfma_f32_16x16x32_bf16 v[86:89], v[176:179], v[200:203], v[86:89]
	v_mfma_f32_16x16x32_bf16 v[78:81], v[160:163], v[208:211], v[78:81]
	v_mfma_f32_16x16x32_bf16 v[70:73], v[176:179], v[208:211], v[70:73]
	s_barrier
	s_add_i32 s48, 0, 0x14000
	s_add_i32 s33, s33, s30
	v_add_u32_e32 v165, s48, v141
	v_lshl_add_u64 v[166:167], s[6:7], 0, v[130:131]
	s_mov_b32 m0, s33
	ds_read_b128 v[212:215], v165
	ds_read_b128 v[230:233], v165 offset:1024
	ds_read_b128 v[234:237], v165 offset:2048
	ds_read_b128 v[238:241], v165 offset:3072
	global_load_lds_dwordx4 v[166:167], off
	v_lshl_add_u64 v[220:221], s[6:7], 0, v[132:133]
	s_add_i32 m0, s33, 0x2000
	s_nop 0
	global_load_lds_dwordx4 v[220:221], off
	s_barrier
	s_waitcnt lgkmcnt(0)
	s_waitcnt lgkmcnt(0)
	v_mfma_f32_16x16x32_bf16 v[122:125], v[212:215], v[180:183], v[122:125]
	v_mfma_f32_16x16x32_bf16 v[114:117], v[234:237], v[180:183], v[114:117]
	v_mfma_f32_16x16x32_bf16 v[106:109], v[212:215], v[188:191], v[106:109]
	v_mfma_f32_16x16x32_bf16 v[98:101], v[234:237], v[188:191], v[98:101]
	v_mfma_f32_16x16x32_bf16 v[90:93], v[212:215], v[196:199], v[90:93]
	v_mfma_f32_16x16x32_bf16 v[82:85], v[234:237], v[196:199], v[82:85]
	v_mfma_f32_16x16x32_bf16 v[74:77], v[212:215], v[204:207], v[74:77]
	v_mfma_f32_16x16x32_bf16 v[66:69], v[234:237], v[204:207], v[66:69]
	v_mfma_f32_16x16x32_bf16 v[122:125], v[230:233], v[184:187], v[122:125]
	v_mfma_f32_16x16x32_bf16 v[114:117], v[238:241], v[184:187], v[114:117]
	v_mfma_f32_16x16x32_bf16 v[106:109], v[230:233], v[192:195], v[106:109]
	v_mfma_f32_16x16x32_bf16 v[98:101], v[238:241], v[192:195], v[98:101]
	v_mfma_f32_16x16x32_bf16 v[90:93], v[230:233], v[200:203], v[90:93]
	v_mfma_f32_16x16x32_bf16 v[82:85], v[238:241], v[200:203], v[82:85]
	v_mfma_f32_16x16x32_bf16 v[74:77], v[230:233], v[208:211], v[74:77]
	v_mfma_f32_16x16x32_bf16 v[66:69], v[238:241], v[208:211], v[66:69]
	s_mov_b32 m0, s31
	s_barrier
	ds_read_b128 v[180:183], v151 offset:16384
	ds_read_b128 v[184:187], v151 offset:17408
	ds_read_b128 v[188:191], v151 offset:18432
	ds_read_b128 v[192:195], v151 offset:19456
	ds_read_b128 v[196:199], v151 offset:20480
	ds_read_b128 v[200:203], v151 offset:21504
	ds_read_b128 v[204:207], v151 offset:22528
	ds_read_b128 v[208:211], v151 offset:23552
	global_load_lds_dwordx4 v226, s[24:25]
	s_mov_b32 m0, s34
	v_mov_b32_e32 v165, v227
	global_load_lds_dwordx4 v164, s[24:25]
	s_barrier
	s_waitcnt lgkmcnt(0)
	v_lshl_add_u64 v[222:223], s[24:25], 0, v[226:227]
	v_lshl_add_u64 v[164:165], s[24:25], 0, v[164:165]
	s_waitcnt lgkmcnt(0)
	v_mfma_f32_16x16x32_bf16 v[58:61], v[156:159], v[180:183], v[58:61]
	v_mfma_f32_16x16x32_bf16 v[50:53], v[172:175], v[180:183], v[50:53]
	v_mfma_f32_16x16x32_bf16 v[42:45], v[156:159], v[188:191], v[42:45]
	v_mfma_f32_16x16x32_bf16 v[34:37], v[172:175], v[188:191], v[34:37]
	v_mfma_f32_16x16x32_bf16 v[26:29], v[156:159], v[196:199], v[26:29]
	v_mfma_f32_16x16x32_bf16 v[18:21], v[172:175], v[196:199], v[18:21]
	v_mfma_f32_16x16x32_bf16 v[6:9], v[156:159], v[204:207], v[6:9]
	v_mfma_f32_16x16x32_bf16 v[2:5], v[172:175], v[204:207], v[2:5]
	v_mfma_f32_16x16x32_bf16 v[58:61], v[160:163], v[184:187], v[58:61]
	v_mfma_f32_16x16x32_bf16 v[50:53], v[176:179], v[184:187], v[50:53]
	v_mfma_f32_16x16x32_bf16 v[42:45], v[160:163], v[192:195], v[42:45]
	v_mfma_f32_16x16x32_bf16 v[34:37], v[176:179], v[192:195], v[34:37]
	v_mfma_f32_16x16x32_bf16 v[26:29], v[160:163], v[200:203], v[26:29]
	v_mfma_f32_16x16x32_bf16 v[18:21], v[176:179], v[200:203], v[18:21]
	v_mfma_f32_16x16x32_bf16 v[6:9], v[160:163], v[208:211], v[6:9]
	v_mfma_f32_16x16x32_bf16 v[2:5], v[176:179], v[208:211], v[2:5]
	s_barrier
	s_add_u32 s46, s6, 0x40000
	s_addc_u32 s47, s7, 0
	s_add_i32 s33, s48, s30
	v_lshl_add_u64 v[156:157], s[46:47], 0, v[130:131]
	s_mov_b32 m0, s33
	s_nop 0
	global_load_lds_dwordx4 v[156:157], off
	v_lshl_add_u64 v[156:157], s[46:47], 0, v[132:133]
	s_add_i32 m0, s33, 0x2000
	s_nop 0
	global_load_lds_dwordx4 v[156:157], off
	s_waitcnt vmcnt(6)
	s_barrier
	v_mfma_f32_16x16x32_bf16 v[62:65], v[212:215], v[180:183], v[62:65]
	v_mfma_f32_16x16x32_bf16 v[54:57], v[234:237], v[180:183], v[54:57]
	v_mfma_f32_16x16x32_bf16 v[46:49], v[212:215], v[188:191], v[46:49]
	v_mfma_f32_16x16x32_bf16 v[38:41], v[234:237], v[188:191], v[38:41]
	v_mfma_f32_16x16x32_bf16 v[30:33], v[212:215], v[196:199], v[30:33]
	v_mfma_f32_16x16x32_bf16 v[22:25], v[234:237], v[196:199], v[22:25]
	v_mfma_f32_16x16x32_bf16 v[14:17], v[212:215], v[204:207], v[14:17]
	v_mfma_f32_16x16x32_bf16 v[10:13], v[234:237], v[204:207], v[10:13]
	v_mfma_f32_16x16x32_bf16 v[62:65], v[230:233], v[184:187], v[62:65]
	v_mfma_f32_16x16x32_bf16 v[54:57], v[238:241], v[184:187], v[54:57]
	v_mfma_f32_16x16x32_bf16 v[46:49], v[230:233], v[192:195], v[46:49]
	v_mfma_f32_16x16x32_bf16 v[38:41], v[238:241], v[192:195], v[38:41]
	v_mfma_f32_16x16x32_bf16 v[30:33], v[230:233], v[200:203], v[30:33]
	v_mfma_f32_16x16x32_bf16 v[22:25], v[238:241], v[200:203], v[22:25]
	v_mfma_f32_16x16x32_bf16 v[14:17], v[230:233], v[208:211], v[14:17]
	v_mfma_f32_16x16x32_bf16 v[10:13], v[238:241], v[208:211], v[10:13]
	s_add_i32 s33, 0, 0x18000
	v_add_u32_e32 v171, s33, v141
	s_barrier
	ds_read_b128 v[156:159], v171
	ds_read_b128 v[160:163], v171 offset:1024
	ds_read_b128 v[172:175], v171 offset:2048
	ds_read_b128 v[176:179], v171 offset:3072
	s_mov_b32 m0, s35
	ds_read_b128 v[180:183], v151 offset:32768
	ds_read_b128 v[184:187], v151 offset:33792
	ds_read_b128 v[188:191], v151 offset:34816
	ds_read_b128 v[192:195], v151 offset:35840
	ds_read_b128 v[196:199], v151 offset:36864
	ds_read_b128 v[200:203], v151 offset:37888
	ds_read_b128 v[204:207], v151 offset:38912
	ds_read_b128 v[208:211], v151 offset:39936
	global_load_lds_dwordx4 v135, s[24:25]
	s_mov_b32 m0, s36
	s_nop 0
	global_load_lds_dwordx4 v137, s[24:25]
	s_waitcnt lgkmcnt(8)
	s_barrier
	s_waitcnt lgkmcnt(0)
	s_waitcnt lgkmcnt(0)
	v_mfma_f32_16x16x32_bf16 v[126:129], v[156:159], v[180:183], v[126:129]
	v_mfma_f32_16x16x32_bf16 v[118:121], v[172:175], v[180:183], v[118:121]
	v_mfma_f32_16x16x32_bf16 v[110:113], v[156:159], v[188:191], v[110:113]
	v_mfma_f32_16x16x32_bf16 v[102:105], v[172:175], v[188:191], v[102:105]
	v_mfma_f32_16x16x32_bf16 v[94:97], v[156:159], v[196:199], v[94:97]
	v_mfma_f32_16x16x32_bf16 v[86:89], v[172:175], v[196:199], v[86:89]
	v_mfma_f32_16x16x32_bf16 v[78:81], v[156:159], v[204:207], v[78:81]
	v_mfma_f32_16x16x32_bf16 v[70:73], v[172:175], v[204:207], v[70:73]
	v_mfma_f32_16x16x32_bf16 v[126:129], v[160:163], v[184:187], v[126:129]
	v_mfma_f32_16x16x32_bf16 v[118:121], v[176:179], v[184:187], v[118:121]
	v_mfma_f32_16x16x32_bf16 v[110:113], v[160:163], v[192:195], v[110:113]
	v_mfma_f32_16x16x32_bf16 v[102:105], v[176:179], v[192:195], v[102:105]
	v_mfma_f32_16x16x32_bf16 v[94:97], v[160:163], v[200:203], v[94:97]
	v_mfma_f32_16x16x32_bf16 v[86:89], v[176:179], v[200:203], v[86:89]
	v_mfma_f32_16x16x32_bf16 v[78:81], v[160:163], v[208:211], v[78:81]
	v_mfma_f32_16x16x32_bf16 v[70:73], v[176:179], v[208:211], v[70:73]
	s_barrier
	s_add_i32 s24, 0, 0x1c000
	s_add_i32 s25, s33, s30
	v_add_u32_e32 v135, s24, v141
	v_lshl_add_u64 v[166:167], v[166:167], 0, s[96:97]
	s_mov_b32 m0, s25
	ds_read_b128 v[212:215], v135
	ds_read_b128 v[230:233], v135 offset:1024
	ds_read_b128 v[234:237], v135 offset:2048
	ds_read_b128 v[238:241], v135 offset:3072
	global_load_lds_dwordx4 v[166:167], off
	v_lshl_add_u64 v[166:167], v[220:221], 0, s[96:97]
	s_add_i32 m0, s25, 0x2000
	s_nop 0
	global_load_lds_dwordx4 v[166:167], off
	s_barrier
	s_waitcnt lgkmcnt(0)
	s_waitcnt lgkmcnt(0)
	v_mfma_f32_16x16x32_bf16 v[122:125], v[212:215], v[180:183], v[122:125]
	v_mfma_f32_16x16x32_bf16 v[114:117], v[234:237], v[180:183], v[114:117]
	v_mfma_f32_16x16x32_bf16 v[106:109], v[212:215], v[188:191], v[106:109]
	v_mfma_f32_16x16x32_bf16 v[98:101], v[234:237], v[188:191], v[98:101]
	v_mfma_f32_16x16x32_bf16 v[90:93], v[212:215], v[196:199], v[90:93]
	v_mfma_f32_16x16x32_bf16 v[82:85], v[234:237], v[196:199], v[82:85]
	v_mfma_f32_16x16x32_bf16 v[74:77], v[212:215], v[204:207], v[74:77]
	v_mfma_f32_16x16x32_bf16 v[66:69], v[234:237], v[204:207], v[66:69]
	v_mfma_f32_16x16x32_bf16 v[122:125], v[230:233], v[184:187], v[122:125]
	v_mfma_f32_16x16x32_bf16 v[114:117], v[238:241], v[184:187], v[114:117]
	v_mfma_f32_16x16x32_bf16 v[106:109], v[230:233], v[192:195], v[106:109]
	v_mfma_f32_16x16x32_bf16 v[98:101], v[238:241], v[192:195], v[98:101]
	v_mfma_f32_16x16x32_bf16 v[90:93], v[230:233], v[200:203], v[90:93]
	v_mfma_f32_16x16x32_bf16 v[82:85], v[238:241], v[200:203], v[82:85]
	v_mfma_f32_16x16x32_bf16 v[74:77], v[230:233], v[208:211], v[74:77]
	v_mfma_f32_16x16x32_bf16 v[66:69], v[238:241], v[208:211], v[66:69]
	s_mov_b32 m0, s37
	v_lshl_add_u64 v[166:167], v[222:223], 0, s[96:97]
	s_barrier
	ds_read_b128 v[180:183], v151 offset:49152
	ds_read_b128 v[184:187], v151 offset:50176
	ds_read_b128 v[188:191], v151 offset:51200
	ds_read_b128 v[192:195], v151 offset:52224
	ds_read_b128 v[196:199], v151 offset:53248
	ds_read_b128 v[200:203], v151 offset:54272
	ds_read_b128 v[204:207], v151 offset:55296
	ds_read_b128 v[208:211], v151 offset:56320
	global_load_lds_dwordx4 v[166:167], off
	v_lshl_add_u64 v[164:165], v[164:165], 0, s[96:97]
	s_mov_b32 m0, s38
	s_nop 0
	global_load_lds_dwordx4 v[164:165], off
	s_barrier
	s_waitcnt lgkmcnt(0)
	s_waitcnt lgkmcnt(0)
	v_mfma_f32_16x16x32_bf16 v[58:61], v[156:159], v[180:183], v[58:61]
	v_mfma_f32_16x16x32_bf16 v[50:53], v[172:175], v[180:183], v[50:53]
	v_mfma_f32_16x16x32_bf16 v[42:45], v[156:159], v[188:191], v[42:45]
	v_mfma_f32_16x16x32_bf16 v[34:37], v[172:175], v[188:191], v[34:37]
	v_mfma_f32_16x16x32_bf16 v[26:29], v[156:159], v[196:199], v[26:29]
	v_mfma_f32_16x16x32_bf16 v[18:21], v[172:175], v[196:199], v[18:21]
	v_mfma_f32_16x16x32_bf16 v[6:9], v[156:159], v[204:207], v[6:9]
	v_mfma_f32_16x16x32_bf16 v[2:5], v[172:175], v[204:207], v[2:5]
	v_mfma_f32_16x16x32_bf16 v[58:61], v[160:163], v[184:187], v[58:61]
	v_mfma_f32_16x16x32_bf16 v[50:53], v[176:179], v[184:187], v[50:53]
	v_mfma_f32_16x16x32_bf16 v[42:45], v[160:163], v[192:195], v[42:45]
	v_mfma_f32_16x16x32_bf16 v[34:37], v[176:179], v[192:195], v[34:37]
	v_mfma_f32_16x16x32_bf16 v[26:29], v[160:163], v[200:203], v[26:29]
	v_mfma_f32_16x16x32_bf16 v[18:21], v[176:179], v[200:203], v[18:21]
	v_mfma_f32_16x16x32_bf16 v[6:9], v[160:163], v[208:211], v[6:9]
	v_mfma_f32_16x16x32_bf16 v[2:5], v[176:179], v[208:211], v[2:5]
	s_barrier
	s_add_u32 s6, s6, 0x40080
	s_addc_u32 s7, s7, 0
	s_add_i32 s24, s24, s30
	v_lshl_add_u64 v[156:157], s[6:7], 0, v[130:131]
	s_mov_b32 m0, s24
	s_nop 0
	global_load_lds_dwordx4 v[156:157], off
	v_lshl_add_u64 v[156:157], s[6:7], 0, v[132:133]
	s_add_i32 m0, s24, 0x2000
	s_nop 0
	global_load_lds_dwordx4 v[156:157], off
	s_waitcnt vmcnt(6)
	s_barrier
	v_mfma_f32_16x16x32_bf16 v[62:65], v[212:215], v[180:183], v[62:65]
	v_mfma_f32_16x16x32_bf16 v[54:57], v[234:237], v[180:183], v[54:57]
	v_mfma_f32_16x16x32_bf16 v[46:49], v[212:215], v[188:191], v[46:49]
	v_mfma_f32_16x16x32_bf16 v[38:41], v[234:237], v[188:191], v[38:41]
	v_mfma_f32_16x16x32_bf16 v[30:33], v[212:215], v[196:199], v[30:33]
	v_mfma_f32_16x16x32_bf16 v[22:25], v[234:237], v[196:199], v[22:25]
	v_mfma_f32_16x16x32_bf16 v[14:17], v[212:215], v[204:207], v[14:17]
	v_mfma_f32_16x16x32_bf16 v[10:13], v[234:237], v[204:207], v[10:13]
	v_mfma_f32_16x16x32_bf16 v[62:65], v[230:233], v[184:187], v[62:65]
	v_mfma_f32_16x16x32_bf16 v[54:57], v[238:241], v[184:187], v[54:57]
	v_mfma_f32_16x16x32_bf16 v[46:49], v[230:233], v[192:195], v[46:49]
	v_mfma_f32_16x16x32_bf16 v[38:41], v[238:241], v[192:195], v[38:41]
	v_mfma_f32_16x16x32_bf16 v[30:33], v[230:233], v[200:203], v[30:33]
	v_mfma_f32_16x16x32_bf16 v[22:25], v[238:241], v[200:203], v[22:25]
	v_mfma_f32_16x16x32_bf16 v[14:17], v[230:233], v[208:211], v[14:17]
	v_mfma_f32_16x16x32_bf16 v[10:13], v[238:241], v[208:211], v[10:13]
	s_add_i32 s45, s45, 2
	s_add_u32 s0, s0, 0x100
	s_addc_u32 s1, s1, 0
	s_cmp_gt_u32 s45, 13
	s_barrier
	s_cbranch_scc0 .LBB0_1246
	v_lshl_add_u32 v134, s42, 8, v139
	v_ashrrev_i32_e32 v135, 31, v134
	v_lshlrev_b64 v[142:143], 11, v[134:135]
	v_mul_f32_e32 v135, 0xbfb8aa3b, v126
	v_exp_f32_e32 v135, v135
	v_lshl_or_b32 v136, s43, 7, v150
	v_ashrrev_i32_e32 v137, 31, v136
	v_lshl_add_u64 v[142:143], s[16:17], 0, v[142:143]
	v_add_f32_e32 v135, 1.0, v135
	v_rcp_f32_e32 v135, v135
	s_mov_b32 s0, 0x40000
	v_mov_b32_e32 v138, v153
	v_mov_b32_e32 v140, v152
	v_mul_f32_e32 v126, v126, v135
	v_mul_f32_e32 v122, v126, v122
	v_mul_f32_e32 v126, 0xbfb8aa3b, v127
	v_exp_f32_e32 v126, v126
	s_mov_b32 s43, s22
	s_mov_b32 s42, s41
	v_add_f32_e32 v126, 1.0, v126
	v_rcp_f32_e32 v126, v126
	s_nop 0
	v_mul_f32_e32 v126, v127, v126
	v_mul_f32_e32 v123, v126, v123
	v_mul_f32_e32 v126, 0xbfb8aa3b, v128
	v_exp_f32_e32 v126, v126
	s_nop 0
	v_add_f32_e32 v126, 1.0, v126
	v_rcp_f32_e32 v126, v126
	s_nop 0
	v_mul_f32_e32 v126, v128, v126
	v_mul_f32_e32 v124, v126, v124
	v_mul_f32_e32 v126, 0xbfb8aa3b, v129
	v_exp_f32_e32 v126, v126
	s_nop 0
	v_add_f32_e32 v126, 1.0, v126
	v_rcp_f32_e32 v126, v126
	s_nop 0
	v_mul_f32_e32 v126, v129, v126
	v_mul_f32_e32 v125, v126, v125
	v_mul_f32_e32 v126, 0xbfb8aa3b, v118
	v_exp_f32_e32 v126, v126
	s_nop 0
	v_add_f32_e32 v126, 1.0, v126
	v_rcp_f32_e32 v126, v126
	s_nop 0
	v_mul_f32_e32 v118, v118, v126
	v_mul_f32_e32 v126, v118, v114
	v_mul_f32_e32 v114, 0xbfb8aa3b, v119
	v_exp_f32_e32 v114, v114
	v_cvt_pk_bf16_f32 v118, v122, v123
	s_nop 0
	v_add_f32_e32 v114, 1.0, v114
	v_rcp_f32_e32 v114, v114
	s_nop 0
	v_mul_f32_e32 v114, v119, v114
	v_mul_f32_e32 v127, v114, v115
	v_mul_f32_e32 v114, 0xbfb8aa3b, v120
	v_exp_f32_e32 v114, v114
	v_cvt_pk_bf16_f32 v119, v124, v125
	s_nop 0
	v_add_f32_e32 v114, 1.0, v114
	v_rcp_f32_e32 v114, v114
	s_nop 0
	v_mul_f32_e32 v114, v120, v114
	v_mul_f32_e32 v128, v114, v116
	v_mul_f32_e32 v114, 0xbfb8aa3b, v121
	v_exp_f32_e32 v114, v114
	v_cvt_pk_bf16_f32 v120, v126, v127
	s_nop 0
	v_add_f32_e32 v114, 1.0, v114
	v_rcp_f32_e32 v114, v114
	s_nop 0
	v_mul_f32_e32 v114, v121, v114
	v_mul_f32_e32 v121, v114, v117
	v_lshlrev_b64 v[116:117], 1, v[136:137]
	v_lshl_add_u64 v[114:115], v[142:143], 0, v[116:117]
	v_cvt_pk_bf16_f32 v121, v128, v121
	global_store_dwordx4 v[114:115], v[118:121], off
	v_mov_b32_e32 v136, v154
	s_nop 0
	v_mul_f32_e32 v120, 0xbfb8aa3b, v110
	v_exp_f32_e32 v120, v120
	v_or_b32_e32 v118, 16, v134
	v_ashrrev_i32_e32 v119, 31, v118
	v_lshlrev_b64 v[118:119], 11, v[118:119]
	v_add_f32_e32 v120, 1.0, v120
	v_rcp_f32_e32 v120, v120
	v_lshl_add_u64 v[118:119], s[16:17], 0, v[118:119]
	v_mul_f32_e32 v110, v110, v120
	v_mul_f32_e32 v106, v110, v106
	v_mul_f32_e32 v110, 0xbfb8aa3b, v111
	v_exp_f32_e32 v110, v110
	s_nop 0
	v_add_f32_e32 v110, 1.0, v110
	v_rcp_f32_e32 v110, v110
	s_nop 0
	v_mul_f32_e32 v110, v111, v110
	v_mul_f32_e32 v107, v110, v107
	v_mul_f32_e32 v110, 0xbfb8aa3b, v112
	v_exp_f32_e32 v110, v110
	s_nop 0
	v_add_f32_e32 v110, 1.0, v110
	v_rcp_f32_e32 v110, v110
	s_nop 0
	v_mul_f32_e32 v110, v112, v110
	v_mul_f32_e32 v108, v110, v108
	v_mul_f32_e32 v110, 0xbfb8aa3b, v113
	v_exp_f32_e32 v110, v110
	s_nop 0
	v_add_f32_e32 v110, 1.0, v110
	v_rcp_f32_e32 v110, v110
	s_nop 0
	v_mul_f32_e32 v110, v113, v110
	v_mul_f32_e32 v109, v110, v109
	v_mul_f32_e32 v110, 0xbfb8aa3b, v102
	v_exp_f32_e32 v110, v110
	s_nop 0
	v_add_f32_e32 v110, 1.0, v110
	v_rcp_f32_e32 v110, v110
	s_nop 0
	v_mul_f32_e32 v102, v102, v110
	v_mul_f32_e32 v110, v102, v98
	v_mul_f32_e32 v98, 0xbfb8aa3b, v103
	v_exp_f32_e32 v98, v98
	s_nop 0
	v_add_f32_e32 v98, 1.0, v98
	v_rcp_f32_e32 v98, v98
	s_nop 0
	v_mul_f32_e32 v98, v103, v98
	v_mul_f32_e32 v111, v98, v99
	v_mul_f32_e32 v98, 0xbfb8aa3b, v104
	v_exp_f32_e32 v98, v98
	v_lshl_add_u64 v[102:103], v[118:119], 0, v[116:117]
	v_add_f32_e32 v98, 1.0, v98
	v_rcp_f32_e32 v98, v98
	s_nop 0
	v_mul_f32_e32 v98, v104, v98
	v_mul_f32_e32 v104, v98, v100
	v_mul_f32_e32 v98, 0xbfb8aa3b, v105
	v_exp_f32_e32 v98, v98
	s_nop 0
	v_add_f32_e32 v98, 1.0, v98
	v_rcp_f32_e32 v98, v98
	s_nop 0
	v_mul_f32_e32 v98, v105, v98
	v_mul_f32_e32 v101, v98, v101
	v_cvt_pk_bf16_f32 v98, v106, v107
	v_cvt_pk_bf16_f32 v99, v108, v109
	v_cvt_pk_bf16_f32 v100, v110, v111
	v_cvt_pk_bf16_f32 v101, v104, v101
	global_store_dwordx4 v[102:103], v[98:101], off
	s_nop 1
	v_mul_f32_e32 v100, 0xbfb8aa3b, v94
	v_exp_f32_e32 v100, v100
	v_or_b32_e32 v98, 32, v134
	v_ashrrev_i32_e32 v99, 31, v98
	v_lshlrev_b64 v[98:99], 11, v[98:99]
	v_add_f32_e32 v100, 1.0, v100
	v_rcp_f32_e32 v100, v100
	v_lshl_add_u64 v[98:99], s[16:17], 0, v[98:99]
	v_mul_f32_e32 v94, v94, v100
	v_mul_f32_e32 v90, v94, v90
	v_mul_f32_e32 v94, 0xbfb8aa3b, v95
	v_exp_f32_e32 v94, v94
	s_nop 0
	v_add_f32_e32 v94, 1.0, v94
	v_rcp_f32_e32 v94, v94
	s_nop 0
	v_mul_f32_e32 v94, v95, v94
	v_mul_f32_e32 v91, v94, v91
	v_mul_f32_e32 v94, 0xbfb8aa3b, v96
	v_exp_f32_e32 v94, v94
	s_nop 0
	v_add_f32_e32 v94, 1.0, v94
	v_rcp_f32_e32 v94, v94
	s_nop 0
	v_mul_f32_e32 v94, v96, v94
	v_mul_f32_e32 v92, v94, v92
	v_mul_f32_e32 v94, 0xbfb8aa3b, v97
	v_exp_f32_e32 v94, v94
	s_nop 0
	v_add_f32_e32 v94, 1.0, v94
	v_rcp_f32_e32 v94, v94
	s_nop 0
	v_mul_f32_e32 v94, v97, v94
	v_mul_f32_e32 v93, v94, v93
	v_mul_f32_e32 v94, 0xbfb8aa3b, v86
	v_exp_f32_e32 v94, v94
	s_nop 0
	v_add_f32_e32 v94, 1.0, v94
	v_rcp_f32_e32 v94, v94
	s_nop 0
	v_mul_f32_e32 v86, v86, v94
	v_mul_f32_e32 v94, v86, v82
	v_mul_f32_e32 v82, 0xbfb8aa3b, v87
	v_exp_f32_e32 v82, v82
	s_nop 0
	v_add_f32_e32 v82, 1.0, v82
	v_rcp_f32_e32 v82, v82
	s_nop 0
	v_mul_f32_e32 v82, v87, v82
	v_mul_f32_e32 v95, v82, v83
	v_mul_f32_e32 v82, 0xbfb8aa3b, v88
	v_exp_f32_e32 v82, v82
	v_lshl_add_u64 v[86:87], v[98:99], 0, v[116:117]
	v_add_f32_e32 v82, 1.0, v82
	v_rcp_f32_e32 v82, v82
	s_nop 0
	v_mul_f32_e32 v82, v88, v82
	v_mul_f32_e32 v88, v82, v84
	v_mul_f32_e32 v82, 0xbfb8aa3b, v89
	v_exp_f32_e32 v82, v82
	s_nop 0
	v_add_f32_e32 v82, 1.0, v82
	v_rcp_f32_e32 v82, v82
	s_nop 0
	v_mul_f32_e32 v82, v89, v82
	v_mul_f32_e32 v85, v82, v85
	v_cvt_pk_bf16_f32 v82, v90, v91
	v_cvt_pk_bf16_f32 v83, v92, v93
	v_cvt_pk_bf16_f32 v84, v94, v95
	v_cvt_pk_bf16_f32 v85, v88, v85
	global_store_dwordx4 v[86:87], v[82:85], off
	s_nop 1
	v_mul_f32_e32 v84, 0xbfb8aa3b, v78
	v_exp_f32_e32 v84, v84
	v_or_b32_e32 v82, 48, v134
	v_ashrrev_i32_e32 v83, 31, v82
	v_lshlrev_b64 v[82:83], 11, v[82:83]
	v_add_f32_e32 v84, 1.0, v84
	v_rcp_f32_e32 v84, v84
	v_lshl_add_u64 v[82:83], s[16:17], 0, v[82:83]
	v_mov_b32_e32 v134, v155
	v_mul_f32_e32 v78, v78, v84
	v_mul_f32_e32 v74, v78, v74
	v_mul_f32_e32 v78, 0xbfb8aa3b, v79
	v_exp_f32_e32 v78, v78
	s_nop 0
	v_add_f32_e32 v78, 1.0, v78
	v_rcp_f32_e32 v78, v78
	s_nop 0
	v_mul_f32_e32 v78, v79, v78
	v_mul_f32_e32 v75, v78, v75
	v_mul_f32_e32 v78, 0xbfb8aa3b, v80
	v_exp_f32_e32 v78, v78
	s_nop 0
	v_add_f32_e32 v78, 1.0, v78
	v_rcp_f32_e32 v78, v78
	s_nop 0
	v_mul_f32_e32 v78, v80, v78
	v_mul_f32_e32 v76, v78, v76
	v_mul_f32_e32 v78, 0xbfb8aa3b, v81
	v_exp_f32_e32 v78, v78
	s_nop 0
	v_add_f32_e32 v78, 1.0, v78
	v_rcp_f32_e32 v78, v78
	s_nop 0
	v_mul_f32_e32 v78, v81, v78
	v_mul_f32_e32 v77, v78, v77
	v_mul_f32_e32 v78, 0xbfb8aa3b, v70
	v_exp_f32_e32 v78, v78
	s_nop 0
	v_add_f32_e32 v78, 1.0, v78
	v_rcp_f32_e32 v78, v78
	s_nop 0
	v_mul_f32_e32 v70, v70, v78
	v_mul_f32_e32 v78, v70, v66
	v_mul_f32_e32 v66, 0xbfb8aa3b, v71
	v_exp_f32_e32 v66, v66
	s_nop 0
	v_add_f32_e32 v66, 1.0, v66
	v_rcp_f32_e32 v66, v66
	s_nop 0
	v_mul_f32_e32 v66, v71, v66
	v_mul_f32_e32 v79, v66, v67
	v_mul_f32_e32 v66, 0xbfb8aa3b, v72
	v_exp_f32_e32 v66, v66
	v_lshl_add_u64 v[70:71], v[82:83], 0, v[116:117]
	v_add_f32_e32 v66, 1.0, v66
	v_rcp_f32_e32 v66, v66
	s_nop 0
	v_mul_f32_e32 v66, v72, v66
	v_mul_f32_e32 v72, v66, v68
	v_mul_f32_e32 v66, 0xbfb8aa3b, v73
	v_exp_f32_e32 v66, v66
	s_nop 0
	v_add_f32_e32 v66, 1.0, v66
	v_rcp_f32_e32 v66, v66
	s_nop 0
	v_mul_f32_e32 v66, v73, v66
	v_mul_f32_e32 v69, v66, v69
	v_cvt_pk_bf16_f32 v66, v74, v75
	v_cvt_pk_bf16_f32 v67, v76, v77
	v_cvt_pk_bf16_f32 v68, v78, v79
	v_cvt_pk_bf16_f32 v69, v72, v69
	global_store_dwordx4 v[70:71], v[66:69], off
	s_nop 1
	v_mul_f32_e32 v66, 0xbfb8aa3b, v58
	v_exp_f32_e32 v66, v66
	s_nop 0
	v_add_f32_e32 v66, 1.0, v66
	v_rcp_f32_e32 v66, v66
	s_nop 0
	v_mul_f32_e32 v58, v58, v66
	v_mul_f32_e32 v58, v58, v62
	v_mul_f32_e32 v62, 0xbfb8aa3b, v59
	v_exp_f32_e32 v62, v62
	s_nop 0
	v_add_f32_e32 v62, 1.0, v62
	v_rcp_f32_e32 v62, v62
	s_nop 0
	v_mul_f32_e32 v59, v59, v62
	v_mul_f32_e32 v62, 0xbfb8aa3b, v60
	v_exp_f32_e32 v62, v62
	v_mul_f32_e32 v59, v59, v63
	v_add_f32_e32 v62, 1.0, v62
	v_rcp_f32_e32 v62, v62
	s_nop 0
	v_mul_f32_e32 v60, v60, v62
	v_mul_f32_e32 v62, 0xbfb8aa3b, v61
	v_exp_f32_e32 v62, v62
	v_mul_f32_e32 v60, v60, v64
	v_add_f32_e32 v62, 1.0, v62
	v_rcp_f32_e32 v62, v62
	s_nop 0
	v_mul_f32_e32 v61, v61, v62
	v_mul_f32_e32 v62, 0xbfb8aa3b, v50
	v_exp_f32_e32 v62, v62
	v_mul_f32_e32 v61, v61, v65
	v_add_f32_e32 v62, 1.0, v62
	v_rcp_f32_e32 v62, v62
	s_nop 0
	v_mul_f32_e32 v50, v50, v62
	v_mul_f32_e32 v54, v50, v54
	v_mul_f32_e32 v50, 0xbfb8aa3b, v51
	v_exp_f32_e32 v50, v50
	s_nop 0
	v_add_f32_e32 v50, 1.0, v50
	v_rcp_f32_e32 v50, v50
	s_nop 0
	v_mul_f32_e32 v50, v51, v50
	v_mul_f32_e32 v55, v50, v55
	v_mul_f32_e32 v50, 0xbfb8aa3b, v52
	v_exp_f32_e32 v50, v50
	s_nop 0
	v_add_f32_e32 v50, 1.0, v50
	v_rcp_f32_e32 v50, v50
	s_nop 0
	v_mul_f32_e32 v50, v52, v50
	v_mul_f32_e32 v56, v50, v56
	v_mul_f32_e32 v50, 0xbfb8aa3b, v53
	v_exp_f32_e32 v50, v50
	s_nop 0
	v_add_f32_e32 v50, 1.0, v50
	v_rcp_f32_e32 v50, v50
	s_nop 0
	v_mul_f32_e32 v50, v53, v50
	v_mul_f32_e32 v53, v50, v57
	v_cvt_pk_bf16_f32 v50, v58, v59
	v_cvt_pk_bf16_f32 v51, v60, v61
	v_cvt_pk_bf16_f32 v52, v54, v55
	v_add_co_u32_e32 v54, vcc, s0, v114
	v_cvt_pk_bf16_f32 v53, v56, v53
	s_mov_b32 s0, 0x48000
	s_nop 0
	v_addc_co_u32_e32 v55, vcc, 0, v115, vcc
	global_store_dwordx4 v[54:55], v[50:53], off
	s_nop 1
	v_mul_f32_e32 v50, 0xbfb8aa3b, v42
	v_exp_f32_e32 v50, v50
	s_nop 0
	v_add_f32_e32 v50, 1.0, v50
	v_rcp_f32_e32 v50, v50
	s_nop 0
	v_mul_f32_e32 v42, v42, v50
	v_mul_f32_e32 v42, v42, v46
	v_mul_f32_e32 v46, 0xbfb8aa3b, v43
	v_exp_f32_e32 v46, v46
	s_nop 0
	v_add_f32_e32 v46, 1.0, v46
	v_rcp_f32_e32 v46, v46
	s_nop 0
	v_mul_f32_e32 v43, v43, v46
	v_mul_f32_e32 v46, 0xbfb8aa3b, v44
	v_exp_f32_e32 v46, v46
	v_mul_f32_e32 v43, v43, v47
	v_add_f32_e32 v46, 1.0, v46
	v_rcp_f32_e32 v46, v46
	s_nop 0
	v_mul_f32_e32 v44, v44, v46
	v_mul_f32_e32 v46, 0xbfb8aa3b, v45
	v_exp_f32_e32 v46, v46
	v_mul_f32_e32 v44, v44, v48
	v_add_f32_e32 v46, 1.0, v46
	v_rcp_f32_e32 v46, v46
	s_nop 0
	v_mul_f32_e32 v45, v45, v46
	v_mul_f32_e32 v46, 0xbfb8aa3b, v34
	v_exp_f32_e32 v46, v46
	v_mul_f32_e32 v45, v45, v49
	v_add_f32_e32 v46, 1.0, v46
	v_rcp_f32_e32 v46, v46
	s_nop 0
	v_mul_f32_e32 v34, v34, v46
	v_mul_f32_e32 v38, v34, v38
	v_mul_f32_e32 v34, 0xbfb8aa3b, v35
	v_exp_f32_e32 v34, v34
	s_nop 0
	v_add_f32_e32 v34, 1.0, v34
	v_rcp_f32_e32 v34, v34
	s_nop 0
	v_mul_f32_e32 v34, v35, v34
	v_mul_f32_e32 v39, v34, v39
	v_mul_f32_e32 v34, 0xbfb8aa3b, v36
	v_exp_f32_e32 v34, v34
	s_nop 0
	v_add_f32_e32 v34, 1.0, v34
	v_rcp_f32_e32 v34, v34
	s_nop 0
	v_mul_f32_e32 v34, v36, v34
	v_mul_f32_e32 v40, v34, v40
	v_mul_f32_e32 v34, 0xbfb8aa3b, v37
	v_exp_f32_e32 v34, v34
	s_nop 0
	v_add_f32_e32 v34, 1.0, v34
	v_rcp_f32_e32 v34, v34
	s_nop 0
	v_mul_f32_e32 v34, v37, v34
	v_mul_f32_e32 v37, v34, v41
	v_cvt_pk_bf16_f32 v34, v42, v43
	v_cvt_pk_bf16_f32 v35, v44, v45
	v_cvt_pk_bf16_f32 v36, v38, v39
	v_add_co_u32_e32 v38, vcc, s0, v114
	v_cvt_pk_bf16_f32 v37, v40, v37
	s_mov_b32 s0, 0x50000
	s_nop 0
	v_addc_co_u32_e32 v39, vcc, 0, v115, vcc
	global_store_dwordx4 v[38:39], v[34:37], off
	s_nop 1
	v_mul_f32_e32 v34, 0xbfb8aa3b, v26
	v_exp_f32_e32 v34, v34
	s_nop 0
	v_add_f32_e32 v34, 1.0, v34
	v_rcp_f32_e32 v34, v34
	s_nop 0
	v_mul_f32_e32 v26, v26, v34
	v_mul_f32_e32 v26, v26, v30
	v_mul_f32_e32 v30, 0xbfb8aa3b, v27
	v_exp_f32_e32 v30, v30
	s_nop 0
	v_add_f32_e32 v30, 1.0, v30
	v_rcp_f32_e32 v30, v30
	s_nop 0
	v_mul_f32_e32 v27, v27, v30
	v_mul_f32_e32 v30, 0xbfb8aa3b, v28
	v_exp_f32_e32 v30, v30
	v_mul_f32_e32 v27, v27, v31
	v_add_f32_e32 v30, 1.0, v30
	v_rcp_f32_e32 v30, v30
	s_nop 0
	v_mul_f32_e32 v28, v28, v30
	v_mul_f32_e32 v30, 0xbfb8aa3b, v29
	v_exp_f32_e32 v30, v30
	v_mul_f32_e32 v28, v28, v32
	v_add_f32_e32 v30, 1.0, v30
	v_rcp_f32_e32 v30, v30
	s_nop 0
	v_mul_f32_e32 v29, v29, v30
	v_mul_f32_e32 v30, 0xbfb8aa3b, v18
	v_exp_f32_e32 v30, v30
	v_mul_f32_e32 v29, v29, v33
	v_add_f32_e32 v30, 1.0, v30
	v_rcp_f32_e32 v30, v30
	s_nop 0
	v_mul_f32_e32 v18, v18, v30
	v_mul_f32_e32 v22, v18, v22
	v_mul_f32_e32 v18, 0xbfb8aa3b, v19
	v_exp_f32_e32 v18, v18
	s_nop 0
	v_add_f32_e32 v18, 1.0, v18
	v_rcp_f32_e32 v18, v18
	s_nop 0
	v_mul_f32_e32 v18, v19, v18
	v_mul_f32_e32 v23, v18, v23
	v_mul_f32_e32 v18, 0xbfb8aa3b, v20
	v_exp_f32_e32 v18, v18
	s_nop 0
	v_add_f32_e32 v18, 1.0, v18
	v_rcp_f32_e32 v18, v18
	s_nop 0
	v_mul_f32_e32 v18, v20, v18
	v_mul_f32_e32 v24, v18, v24
	v_mul_f32_e32 v18, 0xbfb8aa3b, v21
	v_exp_f32_e32 v18, v18
	s_nop 0
	v_add_f32_e32 v18, 1.0, v18
	v_rcp_f32_e32 v18, v18
	s_nop 0
	v_mul_f32_e32 v18, v21, v18
	v_mul_f32_e32 v21, v18, v25
	v_cvt_pk_bf16_f32 v18, v26, v27
	v_cvt_pk_bf16_f32 v19, v28, v29
	v_cvt_pk_bf16_f32 v20, v22, v23
	v_add_co_u32_e32 v22, vcc, s0, v114
	v_cvt_pk_bf16_f32 v21, v24, v21
	s_mov_b64 s[0:1], s[8:9]
	s_nop 0
	v_addc_co_u32_e32 v23, vcc, 0, v115, vcc
	global_store_dwordx4 v[22:23], v[18:21], off
	s_nop 1
	v_mul_f32_e32 v18, 0xbfb8aa3b, v6
	v_exp_f32_e32 v18, v18
	s_nop 0
	v_add_f32_e32 v18, 1.0, v18
	v_rcp_f32_e32 v18, v18
	s_nop 0
	v_mul_f32_e32 v6, v6, v18
	v_mul_f32_e32 v6, v6, v14
	v_mul_f32_e32 v14, 0xbfb8aa3b, v7
	v_exp_f32_e32 v14, v14
	s_nop 0
	v_add_f32_e32 v14, 1.0, v14
	v_rcp_f32_e32 v14, v14
	s_nop 0
	v_mul_f32_e32 v7, v7, v14
	v_mul_f32_e32 v14, 0xbfb8aa3b, v8
	v_exp_f32_e32 v14, v14
	v_mul_f32_e32 v7, v7, v15
	v_add_f32_e32 v14, 1.0, v14
	v_rcp_f32_e32 v14, v14
	s_nop 0
	v_mul_f32_e32 v8, v8, v14
	v_mul_f32_e32 v14, 0xbfb8aa3b, v9
	v_exp_f32_e32 v14, v14
	v_mul_f32_e32 v8, v8, v16
	v_add_f32_e32 v14, 1.0, v14
	v_rcp_f32_e32 v14, v14
	s_nop 0
	v_mul_f32_e32 v9, v9, v14
	v_mul_f32_e32 v14, 0xbfb8aa3b, v2
	v_exp_f32_e32 v14, v14
	v_mul_f32_e32 v9, v9, v17
	v_add_f32_e32 v14, 1.0, v14
	v_rcp_f32_e32 v14, v14
	s_nop 0
	v_mul_f32_e32 v2, v2, v14
	v_mul_f32_e32 v10, v2, v10
	v_mul_f32_e32 v2, 0xbfb8aa3b, v3
	v_exp_f32_e32 v2, v2
	s_nop 0
	v_add_f32_e32 v2, 1.0, v2
	v_rcp_f32_e32 v2, v2
	s_nop 0
	v_mul_f32_e32 v2, v3, v2
	v_mul_f32_e32 v11, v2, v11
	v_mul_f32_e32 v2, 0xbfb8aa3b, v4
	v_exp_f32_e32 v2, v2
	s_nop 0
	v_add_f32_e32 v2, 1.0, v2
	v_rcp_f32_e32 v2, v2
	s_nop 0
	v_mul_f32_e32 v2, v4, v2
	v_mul_f32_e32 v12, v2, v12
	v_mul_f32_e32 v2, 0xbfb8aa3b, v5
	v_exp_f32_e32 v2, v2
	s_nop 0
	v_add_f32_e32 v2, 1.0, v2
	v_rcp_f32_e32 v2, v2
	s_nop 0
	v_mul_f32_e32 v2, v5, v2
	v_mul_f32_e32 v5, v2, v13
	v_cvt_pk_bf16_f32 v2, v6, v7
	v_add_co_u32_e32 v6, vcc, 0x58000, v114
	v_cvt_pk_bf16_f32 v3, v8, v9
	v_cvt_pk_bf16_f32 v4, v10, v11
	v_cvt_pk_bf16_f32 v5, v12, v5
	s_nop 1
	v_addc_co_u32_e32 v7, vcc, 0, v115, vcc
	s_and_b64 vcc, exec, s[4:5]
	global_store_dwordx4 v[6:7], v[2:5], off
	s_cbranch_vccz .LBB0_1233
	s_branch .LBB0_1252

.LBB0_1327:
	s_add_u32 s24, s8, s22
	s_addc_u32 s25, s9, s23
	s_add_u32 s26, s24, 0x100
	s_addc_u32 s27, s25, 0
	s_add_u32 s33, s19, s22
	s_addc_u32 s52, s48, s23
	s_cmpk_eq_i32 s22, 0x700
	s_cselect_b64 s[50:51], -1, 0
	s_and_b64 s[24:25], s[50:51], exec
	s_cselect_b32 s27, s9, s27
	s_cselect_b32 s26, s8, s26
	s_cselect_b32 s25, s21, s52
	s_cselect_b32 s24, s20, s33
	s_add_i32 s33, 0, 0x10000
	v_add_u32_e32 v137, s33, v148
	ds_read_b128 v[156:159], v137
	ds_read_b128 v[160:163], v137 offset:1024
	ds_read_b128 v[172:175], v137 offset:2048
	ds_read_b128 v[176:179], v137 offset:3072
	s_and_b64 vcc, s[6:7], s[50:51]
	v_cndmask_b32_e32 v226, v134, v151, vcc
	v_cndmask_b32_e32 v164, v136, v152, vcc
	v_cndmask_b32_e32 v137, v140, v153, vcc
	v_cndmask_b32_e32 v139, v138, v154, vcc
	v_lshl_add_u64 v[166:167], v[144:145], 0, s[22:23]
	s_add_i32 m0, s37, 0xc000
	ds_read_b128 v[180:183], v150
	ds_read_b128 v[184:187], v150 offset:1024
	ds_read_b128 v[188:191], v150 offset:2048
	ds_read_b128 v[192:195], v150 offset:3072
	ds_read_b128 v[196:199], v150 offset:4096
	ds_read_b128 v[200:203], v150 offset:5120
	ds_read_b128 v[204:207], v150 offset:6144
	ds_read_b128 v[208:211], v150 offset:7168
	global_load_lds_dwordx4 v[166:167], off
	v_lshl_add_u64 v[166:167], v[142:143], 0, s[22:23]
	s_add_i32 m0, s37, 0xe000
	s_nop 0
	global_load_lds_dwordx4 v[166:167], off
	s_waitcnt lgkmcnt(8)
	s_barrier
	s_waitcnt lgkmcnt(0)
	s_waitcnt lgkmcnt(0)
	v_mfma_f32_16x16x32_bf16 v[126:129], v[156:159], v[180:183], v[126:129]
	v_mfma_f32_16x16x32_bf16 v[122:125], v[172:175], v[180:183], v[122:125]
	v_mfma_f32_16x16x32_bf16 v[114:117], v[156:159], v[188:191], v[114:117]
	v_mfma_f32_16x16x32_bf16 v[106:109], v[172:175], v[188:191], v[106:109]
	v_mfma_f32_16x16x32_bf16 v[98:101], v[156:159], v[196:199], v[98:101]
	v_mfma_f32_16x16x32_bf16 v[90:93], v[172:175], v[196:199], v[90:93]
	v_mfma_f32_16x16x32_bf16 v[82:85], v[156:159], v[204:207], v[82:85]
	v_mfma_f32_16x16x32_bf16 v[74:77], v[172:175], v[204:207], v[74:77]
	v_mfma_f32_16x16x32_bf16 v[126:129], v[160:163], v[184:187], v[126:129]
	v_mfma_f32_16x16x32_bf16 v[122:125], v[176:179], v[184:187], v[122:125]
	v_mfma_f32_16x16x32_bf16 v[114:117], v[160:163], v[192:195], v[114:117]
	v_mfma_f32_16x16x32_bf16 v[106:109], v[176:179], v[192:195], v[106:109]
	v_mfma_f32_16x16x32_bf16 v[98:101], v[160:163], v[200:203], v[98:101]
	v_mfma_f32_16x16x32_bf16 v[90:93], v[176:179], v[200:203], v[90:93]
	v_mfma_f32_16x16x32_bf16 v[82:85], v[160:163], v[208:211], v[82:85]
	v_mfma_f32_16x16x32_bf16 v[74:77], v[176:179], v[208:211], v[74:77]
	s_barrier
	s_add_i32 s52, 0, 0x14000
	s_add_i32 s33, s33, s36
	v_add_u32_e32 v141, s52, v148
	v_lshl_add_u64 v[166:167], s[24:25], 0, v[130:131]
	s_mov_b32 m0, s33
	ds_read_b128 v[212:215], v141
	ds_read_b128 v[230:233], v141 offset:1024
	ds_read_b128 v[234:237], v141 offset:2048
	ds_read_b128 v[238:241], v141 offset:3072
	global_load_lds_dwordx4 v[166:167], off
	v_lshl_add_u64 v[220:221], s[24:25], 0, v[132:133]
	s_add_i32 m0, s33, 0x2000
	s_nop 0
	global_load_lds_dwordx4 v[220:221], off
	s_barrier
	s_waitcnt lgkmcnt(0)
	s_waitcnt lgkmcnt(0)
	v_mfma_f32_16x16x32_bf16 v[118:121], v[212:215], v[180:183], v[118:121]
	v_mfma_f32_16x16x32_bf16 v[110:113], v[234:237], v[180:183], v[110:113]
	v_mfma_f32_16x16x32_bf16 v[102:105], v[212:215], v[188:191], v[102:105]
	v_mfma_f32_16x16x32_bf16 v[94:97], v[234:237], v[188:191], v[94:97]
	v_mfma_f32_16x16x32_bf16 v[86:89], v[212:215], v[196:199], v[86:89]
	v_mfma_f32_16x16x32_bf16 v[78:81], v[234:237], v[196:199], v[78:81]
	v_mfma_f32_16x16x32_bf16 v[70:73], v[212:215], v[204:207], v[70:73]
	v_mfma_f32_16x16x32_bf16 v[58:61], v[234:237], v[204:207], v[58:61]
	v_mfma_f32_16x16x32_bf16 v[118:121], v[230:233], v[184:187], v[118:121]
	v_mfma_f32_16x16x32_bf16 v[110:113], v[238:241], v[184:187], v[110:113]
	v_mfma_f32_16x16x32_bf16 v[102:105], v[230:233], v[192:195], v[102:105]
	v_mfma_f32_16x16x32_bf16 v[94:97], v[238:241], v[192:195], v[94:97]
	v_mfma_f32_16x16x32_bf16 v[86:89], v[230:233], v[200:203], v[86:89]
	v_mfma_f32_16x16x32_bf16 v[78:81], v[238:241], v[200:203], v[78:81]
	v_mfma_f32_16x16x32_bf16 v[70:73], v[230:233], v[208:211], v[70:73]
	v_mfma_f32_16x16x32_bf16 v[58:61], v[238:241], v[208:211], v[58:61]
	s_mov_b32 m0, s37
	s_barrier
	ds_read_b128 v[180:183], v150 offset:16384
	ds_read_b128 v[184:187], v150 offset:17408
	ds_read_b128 v[188:191], v150 offset:18432
	ds_read_b128 v[192:195], v150 offset:19456
	ds_read_b128 v[196:199], v150 offset:20480
	ds_read_b128 v[200:203], v150 offset:21504
	ds_read_b128 v[204:207], v150 offset:22528
	ds_read_b128 v[208:211], v150 offset:23552
	global_load_lds_dwordx4 v226, s[26:27]
	s_mov_b32 m0, s38
	v_mov_b32_e32 v165, v227
	global_load_lds_dwordx4 v164, s[26:27]
	s_barrier
	s_waitcnt lgkmcnt(0)
	v_lshl_add_u64 v[222:223], s[26:27], 0, v[226:227]
	v_lshl_add_u64 v[164:165], s[26:27], 0, v[164:165]
	s_waitcnt lgkmcnt(0)
	v_mfma_f32_16x16x32_bf16 v[54:57], v[156:159], v[180:183], v[54:57]
	v_mfma_f32_16x16x32_bf16 v[50:53], v[172:175], v[180:183], v[50:53]
	v_mfma_f32_16x16x32_bf16 v[30:33], v[156:159], v[188:191], v[30:33]
	v_mfma_f32_16x16x32_bf16 v[26:29], v[172:175], v[188:191], v[26:29]
	v_mfma_f32_16x16x32_bf16 v[14:17], v[156:159], v[196:199], v[14:17]
	v_mfma_f32_16x16x32_bf16 v[10:13], v[172:175], v[196:199], v[10:13]
	v_mfma_f32_16x16x32_bf16 v[6:9], v[156:159], v[204:207], v[6:9]
	v_mfma_f32_16x16x32_bf16 v[2:5], v[172:175], v[204:207], v[2:5]
	v_mfma_f32_16x16x32_bf16 v[54:57], v[160:163], v[184:187], v[54:57]
	v_mfma_f32_16x16x32_bf16 v[50:53], v[176:179], v[184:187], v[50:53]
	v_mfma_f32_16x16x32_bf16 v[30:33], v[160:163], v[192:195], v[30:33]
	v_mfma_f32_16x16x32_bf16 v[26:29], v[176:179], v[192:195], v[26:29]
	v_mfma_f32_16x16x32_bf16 v[14:17], v[160:163], v[200:203], v[14:17]
	v_mfma_f32_16x16x32_bf16 v[10:13], v[176:179], v[200:203], v[10:13]
	v_mfma_f32_16x16x32_bf16 v[6:9], v[160:163], v[208:211], v[6:9]
	v_mfma_f32_16x16x32_bf16 v[2:5], v[176:179], v[208:211], v[2:5]
	s_barrier
	s_add_u32 s50, s24, 0x40000
	s_addc_u32 s51, s25, 0
	s_add_i32 s33, s52, s36
	v_lshl_add_u64 v[156:157], s[50:51], 0, v[130:131]
	s_mov_b32 m0, s33
	s_nop 0
	global_load_lds_dwordx4 v[156:157], off
	v_lshl_add_u64 v[156:157], s[50:51], 0, v[132:133]
	s_add_i32 m0, s33, 0x2000
	s_nop 0
	global_load_lds_dwordx4 v[156:157], off
	s_waitcnt vmcnt(6)
	s_barrier
	v_mfma_f32_16x16x32_bf16 v[62:65], v[212:215], v[180:183], v[62:65]
	v_mfma_f32_16x16x32_bf16 v[66:69], v[234:237], v[180:183], v[66:69]
	v_mfma_f32_16x16x32_bf16 v[42:45], v[212:215], v[188:191], v[42:45]
	v_mfma_f32_16x16x32_bf16 v[46:49], v[234:237], v[188:191], v[46:49]
	v_mfma_f32_16x16x32_bf16 v[34:37], v[212:215], v[196:199], v[34:37]
	v_mfma_f32_16x16x32_bf16 v[38:41], v[234:237], v[196:199], v[38:41]
	v_mfma_f32_16x16x32_bf16 v[18:21], v[212:215], v[204:207], v[18:21]
	v_mfma_f32_16x16x32_bf16 v[22:25], v[234:237], v[204:207], v[22:25]
	v_mfma_f32_16x16x32_bf16 v[62:65], v[230:233], v[184:187], v[62:65]
	v_mfma_f32_16x16x32_bf16 v[66:69], v[238:241], v[184:187], v[66:69]
	v_mfma_f32_16x16x32_bf16 v[42:45], v[230:233], v[192:195], v[42:45]
	v_mfma_f32_16x16x32_bf16 v[46:49], v[238:241], v[192:195], v[46:49]
	v_mfma_f32_16x16x32_bf16 v[34:37], v[230:233], v[200:203], v[34:37]
	v_mfma_f32_16x16x32_bf16 v[38:41], v[238:241], v[200:203], v[38:41]
	v_mfma_f32_16x16x32_bf16 v[18:21], v[230:233], v[208:211], v[18:21]
	v_mfma_f32_16x16x32_bf16 v[22:25], v[238:241], v[208:211], v[22:25]
	s_add_i32 s33, 0, 0x18000
	v_add_u32_e32 v141, s33, v148
	s_barrier
	ds_read_b128 v[156:159], v141
	ds_read_b128 v[160:163], v141 offset:1024
	ds_read_b128 v[172:175], v141 offset:2048
	ds_read_b128 v[176:179], v141 offset:3072
	s_mov_b32 m0, s39
	ds_read_b128 v[180:183], v150 offset:32768
	ds_read_b128 v[184:187], v150 offset:33792
	ds_read_b128 v[188:191], v150 offset:34816
	ds_read_b128 v[192:195], v150 offset:35840
	ds_read_b128 v[196:199], v150 offset:36864
	ds_read_b128 v[200:203], v150 offset:37888
	ds_read_b128 v[204:207], v150 offset:38912
	ds_read_b128 v[208:211], v150 offset:39936
	global_load_lds_dwordx4 v137, s[26:27]
	s_mov_b32 m0, s40
	s_nop 0
	global_load_lds_dwordx4 v139, s[26:27]
	s_waitcnt lgkmcnt(8)
	s_barrier
	s_waitcnt lgkmcnt(0)
	s_waitcnt lgkmcnt(0)
	v_mfma_f32_16x16x32_bf16 v[126:129], v[156:159], v[180:183], v[126:129]
	v_mfma_f32_16x16x32_bf16 v[122:125], v[172:175], v[180:183], v[122:125]
	v_mfma_f32_16x16x32_bf16 v[114:117], v[156:159], v[188:191], v[114:117]
	v_mfma_f32_16x16x32_bf16 v[106:109], v[172:175], v[188:191], v[106:109]
	v_mfma_f32_16x16x32_bf16 v[98:101], v[156:159], v[196:199], v[98:101]
	v_mfma_f32_16x16x32_bf16 v[90:93], v[172:175], v[196:199], v[90:93]
	v_mfma_f32_16x16x32_bf16 v[82:85], v[156:159], v[204:207], v[82:85]
	v_mfma_f32_16x16x32_bf16 v[74:77], v[172:175], v[204:207], v[74:77]
	v_mfma_f32_16x16x32_bf16 v[126:129], v[160:163], v[184:187], v[126:129]
	v_mfma_f32_16x16x32_bf16 v[122:125], v[176:179], v[184:187], v[122:125]
	v_mfma_f32_16x16x32_bf16 v[114:117], v[160:163], v[192:195], v[114:117]
	v_mfma_f32_16x16x32_bf16 v[106:109], v[176:179], v[192:195], v[106:109]
	v_mfma_f32_16x16x32_bf16 v[98:101], v[160:163], v[200:203], v[98:101]
	v_mfma_f32_16x16x32_bf16 v[90:93], v[176:179], v[200:203], v[90:93]
	v_mfma_f32_16x16x32_bf16 v[82:85], v[160:163], v[208:211], v[82:85]
	v_mfma_f32_16x16x32_bf16 v[74:77], v[176:179], v[208:211], v[74:77]
	s_barrier
	s_add_i32 s26, 0, 0x1c000
	s_add_i32 s27, s33, s36
	v_add_u32_e32 v137, s26, v148
	v_lshl_add_u64 v[166:167], v[166:167], 0, s[96:97]
	s_mov_b32 m0, s27
	ds_read_b128 v[212:215], v137
	ds_read_b128 v[230:233], v137 offset:1024
	ds_read_b128 v[234:237], v137 offset:2048
	ds_read_b128 v[238:241], v137 offset:3072
	global_load_lds_dwordx4 v[166:167], off
	v_lshl_add_u64 v[166:167], v[220:221], 0, s[96:97]
	s_add_i32 m0, s27, 0x2000
	s_nop 0
	global_load_lds_dwordx4 v[166:167], off
	s_barrier
	s_waitcnt lgkmcnt(0)
	s_waitcnt lgkmcnt(0)
	v_mfma_f32_16x16x32_bf16 v[118:121], v[212:215], v[180:183], v[118:121]
	v_mfma_f32_16x16x32_bf16 v[110:113], v[234:237], v[180:183], v[110:113]
	v_mfma_f32_16x16x32_bf16 v[102:105], v[212:215], v[188:191], v[102:105]
	v_mfma_f32_16x16x32_bf16 v[94:97], v[234:237], v[188:191], v[94:97]
	v_mfma_f32_16x16x32_bf16 v[86:89], v[212:215], v[196:199], v[86:89]
	v_mfma_f32_16x16x32_bf16 v[78:81], v[234:237], v[196:199], v[78:81]
	v_mfma_f32_16x16x32_bf16 v[70:73], v[212:215], v[204:207], v[70:73]
	v_mfma_f32_16x16x32_bf16 v[58:61], v[234:237], v[204:207], v[58:61]
	v_mfma_f32_16x16x32_bf16 v[118:121], v[230:233], v[184:187], v[118:121]
	v_mfma_f32_16x16x32_bf16 v[110:113], v[238:241], v[184:187], v[110:113]
	v_mfma_f32_16x16x32_bf16 v[102:105], v[230:233], v[192:195], v[102:105]
	v_mfma_f32_16x16x32_bf16 v[94:97], v[238:241], v[192:195], v[94:97]
	v_mfma_f32_16x16x32_bf16 v[86:89], v[230:233], v[200:203], v[86:89]
	v_mfma_f32_16x16x32_bf16 v[78:81], v[238:241], v[200:203], v[78:81]
	v_mfma_f32_16x16x32_bf16 v[70:73], v[230:233], v[208:211], v[70:73]
	v_mfma_f32_16x16x32_bf16 v[58:61], v[238:241], v[208:211], v[58:61]
	s_mov_b32 m0, s41
	v_lshl_add_u64 v[166:167], v[222:223], 0, s[96:97]
	s_barrier
	ds_read_b128 v[180:183], v150 offset:49152
	ds_read_b128 v[184:187], v150 offset:50176
	ds_read_b128 v[188:191], v150 offset:51200
	ds_read_b128 v[192:195], v150 offset:52224
	ds_read_b128 v[196:199], v150 offset:53248
	ds_read_b128 v[200:203], v150 offset:54272
	ds_read_b128 v[204:207], v150 offset:55296
	ds_read_b128 v[208:211], v150 offset:56320
	global_load_lds_dwordx4 v[166:167], off
	v_lshl_add_u64 v[164:165], v[164:165], 0, s[96:97]
	s_mov_b32 m0, s42
	s_nop 0
	global_load_lds_dwordx4 v[164:165], off
	s_barrier
	s_waitcnt lgkmcnt(0)
	s_waitcnt lgkmcnt(0)
	v_mfma_f32_16x16x32_bf16 v[54:57], v[156:159], v[180:183], v[54:57]
	v_mfma_f32_16x16x32_bf16 v[50:53], v[172:175], v[180:183], v[50:53]
	v_mfma_f32_16x16x32_bf16 v[30:33], v[156:159], v[188:191], v[30:33]
	v_mfma_f32_16x16x32_bf16 v[26:29], v[172:175], v[188:191], v[26:29]
	v_mfma_f32_16x16x32_bf16 v[14:17], v[156:159], v[196:199], v[14:17]
	v_mfma_f32_16x16x32_bf16 v[10:13], v[172:175], v[196:199], v[10:13]
	v_mfma_f32_16x16x32_bf16 v[6:9], v[156:159], v[204:207], v[6:9]
	v_mfma_f32_16x16x32_bf16 v[2:5], v[172:175], v[204:207], v[2:5]
	v_mfma_f32_16x16x32_bf16 v[54:57], v[160:163], v[184:187], v[54:57]
	v_mfma_f32_16x16x32_bf16 v[50:53], v[176:179], v[184:187], v[50:53]
	v_mfma_f32_16x16x32_bf16 v[30:33], v[160:163], v[192:195], v[30:33]
	v_mfma_f32_16x16x32_bf16 v[26:29], v[176:179], v[192:195], v[26:29]
	v_mfma_f32_16x16x32_bf16 v[14:17], v[160:163], v[200:203], v[14:17]
	v_mfma_f32_16x16x32_bf16 v[10:13], v[176:179], v[200:203], v[10:13]
	v_mfma_f32_16x16x32_bf16 v[6:9], v[160:163], v[208:211], v[6:9]
	v_mfma_f32_16x16x32_bf16 v[2:5], v[176:179], v[208:211], v[2:5]
	s_barrier
	s_add_u32 s24, s24, 0x40080
	s_addc_u32 s25, s25, 0
	s_add_i32 s26, s26, s36
	v_lshl_add_u64 v[156:157], s[24:25], 0, v[130:131]
	s_mov_b32 m0, s26
	s_nop 0
	global_load_lds_dwordx4 v[156:157], off
	v_lshl_add_u64 v[156:157], s[24:25], 0, v[132:133]
	s_add_i32 m0, s26, 0x2000
	s_nop 0
	global_load_lds_dwordx4 v[156:157], off
	s_waitcnt vmcnt(6)
	s_barrier
	v_mfma_f32_16x16x32_bf16 v[62:65], v[212:215], v[180:183], v[62:65]
	v_mfma_f32_16x16x32_bf16 v[66:69], v[234:237], v[180:183], v[66:69]
	v_mfma_f32_16x16x32_bf16 v[42:45], v[212:215], v[188:191], v[42:45]
	v_mfma_f32_16x16x32_bf16 v[46:49], v[234:237], v[188:191], v[46:49]
	v_mfma_f32_16x16x32_bf16 v[34:37], v[212:215], v[196:199], v[34:37]
	v_mfma_f32_16x16x32_bf16 v[38:41], v[234:237], v[196:199], v[38:41]
	v_mfma_f32_16x16x32_bf16 v[18:21], v[212:215], v[204:207], v[18:21]
	v_mfma_f32_16x16x32_bf16 v[22:25], v[234:237], v[204:207], v[22:25]
	v_mfma_f32_16x16x32_bf16 v[62:65], v[230:233], v[184:187], v[62:65]
	v_mfma_f32_16x16x32_bf16 v[66:69], v[238:241], v[184:187], v[66:69]
	v_mfma_f32_16x16x32_bf16 v[42:45], v[230:233], v[192:195], v[42:45]
	v_mfma_f32_16x16x32_bf16 v[46:49], v[238:241], v[192:195], v[46:49]
	v_mfma_f32_16x16x32_bf16 v[34:37], v[230:233], v[200:203], v[34:37]
	v_mfma_f32_16x16x32_bf16 v[38:41], v[238:241], v[200:203], v[38:41]
	v_mfma_f32_16x16x32_bf16 v[18:21], v[230:233], v[208:211], v[18:21]
	v_mfma_f32_16x16x32_bf16 v[22:25], v[238:241], v[208:211], v[22:25]
	s_add_i32 s49, s49, 2
	s_add_u32 s22, s22, 0x100
	s_addc_u32 s23, s23, 0
	s_cmp_gt_u32 s49, 13
	s_barrier
	s_cbranch_scc0 .LBB0_1327
	v_lshl_add_u32 v136, s46, 8, v135
	v_ashrrev_i32_e32 v137, 31, v136
	v_lshl_add_u64 v[144:145], v[136:137], 2, s[12:13]
	global_load_dword v156, v[144:145], off
	global_load_dword v158, v[144:145], off offset:64
	global_load_dword v160, v[144:145], off offset:128
	global_load_dword v162, v[144:145], off offset:192
	global_load_dword v142, v[144:145], off offset:512
	global_load_dword v140, v[144:145], off offset:576
	global_load_dword v138, v[144:145], off offset:640
	global_load_dword v134, v[144:145], off offset:704
	v_or_b32_e32 v144, 16, v136
	v_or_b32_e32 v164, 32, v136
	v_or_b32_e32 v166, 48, v136
	v_ashrrev_i32_e32 v145, 31, v144
	v_ashrrev_i32_e32 v165, 31, v164
	v_ashrrev_i32_e32 v167, 31, v166
	v_lshl_or_b32 v172, s47, 8, v149
	v_ashrrev_i32_e32 v173, 31, v172
	v_lshlrev_b64 v[136:137], 11, v[136:137]
	v_lshl_add_u64 v[136:137], s[10:11], 0, v[136:137]
	v_lshlrev_b64 v[172:173], 1, v[172:173]
	v_lshl_add_u64 v[136:137], v[136:137], 0, v[172:173]
	s_waitcnt vmcnt(0)
	v_pk_mul_f32 v[128:129], v[128:129], v[156:157] op_sel_hi:[1,0]
	v_pk_mul_f32 v[126:127], v[126:127], v[156:157] op_sel_hi:[1,0]
	v_pk_mul_f32 v[174:175], v[124:125], v[156:157] op_sel_hi:[1,0]
	v_pk_mul_f32 v[124:125], v[122:123], v[156:157] op_sel_hi:[1,0]
	v_cvt_pk_bf16_f32 v122, v126, v127
	v_cvt_pk_bf16_f32 v123, v128, v129
	v_pk_mul_f32 v[120:121], v[120:121], v[156:157] op_sel_hi:[1,0]
	v_cvt_pk_bf16_f32 v124, v124, v125
	v_cvt_pk_bf16_f32 v125, v174, v175
	global_store_dwordx4 v[136:137], v[122:125], off
	v_pk_mul_f32 v[118:119], v[118:119], v[156:157] op_sel_hi:[1,0]
	v_pk_mul_f32 v[114:115], v[114:115], v[158:159] op_sel_hi:[1,0]
	v_pk_mul_f32 v[122:123], v[112:113], v[156:157] op_sel_hi:[1,0]
	v_pk_mul_f32 v[112:113], v[110:111], v[156:157] op_sel_hi:[1,0]
	v_cvt_pk_bf16_f32 v110, v118, v119
	v_cvt_pk_bf16_f32 v111, v120, v121
	v_pk_mul_f32 v[104:105], v[104:105], v[158:159] op_sel_hi:[1,0]
	v_cvt_pk_bf16_f32 v112, v112, v113
	v_cvt_pk_bf16_f32 v113, v122, v123
	global_store_dwordx4 v[136:137], v[110:113], off offset:256
	v_pk_mul_f32 v[102:103], v[102:103], v[158:159] op_sel_hi:[1,0]
	v_pk_mul_f32 v[98:99], v[98:99], v[160:161] op_sel_hi:[1,0]
	v_lshlrev_b64 v[110:111], 11, v[144:145]
	v_lshl_add_u64 v[110:111], s[10:11], 0, v[110:111]
	v_lshl_add_u64 v[110:111], v[110:111], 0, v[172:173]
	v_pk_mul_f32 v[112:113], v[116:117], v[158:159] op_sel_hi:[1,0]
	v_pk_mul_f32 v[116:117], v[108:109], v[158:159] op_sel_hi:[1,0]
	v_pk_mul_f32 v[108:109], v[106:107], v[158:159] op_sel_hi:[1,0]
	v_cvt_pk_bf16_f32 v106, v114, v115
	v_cvt_pk_bf16_f32 v107, v112, v113
	v_pk_mul_f32 v[88:89], v[88:89], v[160:161] op_sel_hi:[1,0]
	v_cvt_pk_bf16_f32 v108, v108, v109
	v_cvt_pk_bf16_f32 v109, v116, v117
	global_store_dwordx4 v[110:111], v[106:109], off
	v_pk_mul_f32 v[86:87], v[86:87], v[160:161] op_sel_hi:[1,0]
	v_pk_mul_f32 v[82:83], v[82:83], v[162:163] op_sel_hi:[1,0]
	v_pk_mul_f32 v[106:107], v[96:97], v[158:159] op_sel_hi:[1,0]
	v_pk_mul_f32 v[96:97], v[94:95], v[158:159] op_sel_hi:[1,0]
	v_cvt_pk_bf16_f32 v94, v102, v103
	v_cvt_pk_bf16_f32 v95, v104, v105
	v_pk_mul_f32 v[72:73], v[72:73], v[162:163] op_sel_hi:[1,0]
	v_cvt_pk_bf16_f32 v96, v96, v97
	v_cvt_pk_bf16_f32 v97, v106, v107
	global_store_dwordx4 v[110:111], v[94:97], off offset:256
	v_pk_mul_f32 v[70:71], v[70:71], v[162:163] op_sel_hi:[1,0]
	v_pk_mul_f32 v[54:55], v[54:55], v[142:143] op_sel_hi:[1,0]
	v_lshlrev_b64 v[94:95], 11, v[164:165]
	v_lshl_add_u64 v[94:95], s[10:11], 0, v[94:95]
	v_lshl_add_u64 v[94:95], v[94:95], 0, v[172:173]
	v_pk_mul_f32 v[96:97], v[100:101], v[160:161] op_sel_hi:[1,0]
	v_pk_mul_f32 v[100:101], v[92:93], v[160:161] op_sel_hi:[1,0]
	v_pk_mul_f32 v[92:93], v[90:91], v[160:161] op_sel_hi:[1,0]
	v_cvt_pk_bf16_f32 v90, v98, v99
	v_cvt_pk_bf16_f32 v91, v96, v97
	s_mov_b32 s6, 0x40000
	v_cvt_pk_bf16_f32 v92, v92, v93
	v_cvt_pk_bf16_f32 v93, v100, v101
	global_store_dwordx4 v[94:95], v[90:93], off
	v_pk_mul_f32 v[56:57], v[56:57], v[142:143] op_sel_hi:[1,0]
	v_pk_mul_f32 v[30:31], v[30:31], v[140:141] op_sel_hi:[1,0]
	v_pk_mul_f32 v[90:91], v[80:81], v[160:161] op_sel_hi:[1,0]
	v_pk_mul_f32 v[80:81], v[78:79], v[160:161] op_sel_hi:[1,0]
	v_cvt_pk_bf16_f32 v78, v86, v87
	v_cvt_pk_bf16_f32 v79, v88, v89
	v_pk_mul_f32 v[32:33], v[32:33], v[140:141] op_sel_hi:[1,0]
	v_cvt_pk_bf16_f32 v80, v80, v81
	v_cvt_pk_bf16_f32 v81, v90, v91
	global_store_dwordx4 v[94:95], v[78:81], off offset:256
	v_pk_mul_f32 v[14:15], v[14:15], v[138:139] op_sel_hi:[1,0]
	v_pk_mul_f32 v[16:17], v[16:17], v[138:139] op_sel_hi:[1,0]
	v_lshlrev_b64 v[78:79], 11, v[166:167]
	v_lshl_add_u64 v[78:79], s[10:11], 0, v[78:79]
	v_lshl_add_u64 v[78:79], v[78:79], 0, v[172:173]
	v_pk_mul_f32 v[80:81], v[84:85], v[162:163] op_sel_hi:[1,0]
	v_pk_mul_f32 v[84:85], v[76:77], v[162:163] op_sel_hi:[1,0]
	v_pk_mul_f32 v[76:77], v[74:75], v[162:163] op_sel_hi:[1,0]
	v_cvt_pk_bf16_f32 v74, v82, v83
	v_cvt_pk_bf16_f32 v75, v80, v81
	v_pk_mul_f32 v[6:7], v[6:7], v[134:135] op_sel_hi:[1,0]
	v_cvt_pk_bf16_f32 v76, v76, v77
	v_cvt_pk_bf16_f32 v77, v84, v85
	global_store_dwordx4 v[78:79], v[74:77], off
	v_pk_mul_f32 v[8:9], v[8:9], v[134:135] op_sel_hi:[1,0]
	s_mov_b32 s47, s18
	v_pk_mul_f32 v[74:75], v[60:61], v[162:163] op_sel_hi:[1,0]
	v_pk_mul_f32 v[60:61], v[58:59], v[162:163] op_sel_hi:[1,0]
	v_cvt_pk_bf16_f32 v58, v70, v71
	v_cvt_pk_bf16_f32 v59, v72, v73
	s_mov_b32 s46, s45
	v_cvt_pk_bf16_f32 v60, v60, v61
	v_cvt_pk_bf16_f32 v61, v74, v75
	global_store_dwordx4 v[78:79], v[58:61], off offset:256
	s_mov_b64 s[22:23], s[20:21]
	s_mov_b32 s49, 0x8000
	v_pk_mul_f32 v[60:61], v[52:53], v[142:143] op_sel_hi:[1,0]
	v_pk_mul_f32 v[52:53], v[50:51], v[142:143] op_sel_hi:[1,0]
	v_cvt_pk_bf16_f32 v50, v54, v55
	v_add_co_u32_e32 v54, vcc, s6, v136
	v_cvt_pk_bf16_f32 v51, v56, v57
	v_cvt_pk_bf16_f32 v52, v52, v53
	v_cvt_pk_bf16_f32 v53, v60, v61
	v_lshl_add_u64 v[58:59], v[136:137], 0, s[94:95]
	s_nop 0
	v_addc_co_u32_e32 v55, vcc, 0, v137, vcc
	global_store_dwordx4 v[54:55], v[50:53], off
	s_mov_b64 s[6:7], 0x48000
	v_pk_mul_f32 v[54:55], v[68:69], v[142:143] op_sel_hi:[1,0]
	v_pk_mul_f32 v[50:51], v[62:63], v[142:143] op_sel_hi:[1,0]
	v_pk_mul_f32 v[52:53], v[64:65], v[142:143] op_sel_hi:[1,0]
	v_cvt_pk_bf16_f32 v50, v50, v51
	v_pk_mul_f32 v[56:57], v[66:67], v[142:143] op_sel_hi:[1,0]
	v_cvt_pk_bf16_f32 v51, v52, v53
	s_nop 0
	v_cvt_pk_bf16_f32 v52, v56, v57
	v_cvt_pk_bf16_f32 v53, v54, v55
	global_store_dwordx4 v[58:59], v[50:53], off offset:256
	s_nop 1
	v_lshl_add_u64 v[50:51], v[136:137], 0, s[6:7]
	s_mov_b32 s6, 0x48000
	v_pk_mul_f32 v[52:53], v[28:29], v[140:141] op_sel_hi:[1,0]
	v_pk_mul_f32 v[28:29], v[26:27], v[140:141] op_sel_hi:[1,0]
	v_cvt_pk_bf16_f32 v26, v30, v31
	v_add_co_u32_e32 v30, vcc, s6, v136
	v_cvt_pk_bf16_f32 v27, v32, v33
	v_cvt_pk_bf16_f32 v28, v28, v29
	v_cvt_pk_bf16_f32 v29, v52, v53
	s_mov_b64 s[6:7], 0x50000
	s_nop 0
	v_addc_co_u32_e32 v31, vcc, 0, v137, vcc
	global_store_dwordx4 v[30:31], v[26:29], off
	v_pk_mul_f32 v[30:31], v[48:49], v[140:141] op_sel_hi:[1,0]
	v_pk_mul_f32 v[32:33], v[46:47], v[140:141] op_sel_hi:[1,0]
	v_pk_mul_f32 v[26:27], v[42:43], v[140:141] op_sel_hi:[1,0]
	v_pk_mul_f32 v[28:29], v[44:45], v[140:141] op_sel_hi:[1,0]
	v_cvt_pk_bf16_f32 v26, v26, v27
	v_mov_b32_e32 v140, v153
	v_cvt_pk_bf16_f32 v27, v28, v29
	v_cvt_pk_bf16_f32 v28, v32, v33
	v_cvt_pk_bf16_f32 v29, v30, v31
	global_store_dwordx4 v[50:51], v[26:29], off offset:256
	s_nop 1
	v_lshl_add_u64 v[26:27], v[136:137], 0, s[6:7]
	s_mov_b32 s6, 0x50000
	v_pk_mul_f32 v[28:29], v[12:13], v[138:139] op_sel_hi:[1,0]
	v_pk_mul_f32 v[12:13], v[10:11], v[138:139] op_sel_hi:[1,0]
	v_cvt_pk_bf16_f32 v10, v14, v15
	v_add_co_u32_e32 v14, vcc, s6, v136
	v_cvt_pk_bf16_f32 v11, v16, v17
	v_cvt_pk_bf16_f32 v12, v12, v13
	v_cvt_pk_bf16_f32 v13, v28, v29
	s_mov_b64 s[6:7], 0x58000
	s_nop 0
	v_addc_co_u32_e32 v15, vcc, 0, v137, vcc
	global_store_dwordx4 v[14:15], v[10:13], off
	v_pk_mul_f32 v[14:15], v[40:41], v[138:139] op_sel_hi:[1,0]
	v_pk_mul_f32 v[16:17], v[38:39], v[138:139] op_sel_hi:[1,0]
	v_pk_mul_f32 v[10:11], v[34:35], v[138:139] op_sel_hi:[1,0]
	v_pk_mul_f32 v[12:13], v[36:37], v[138:139] op_sel_hi:[1,0]
	v_cvt_pk_bf16_f32 v10, v10, v11
	v_mov_b32_e32 v138, v154
	v_cvt_pk_bf16_f32 v11, v12, v13
	v_cvt_pk_bf16_f32 v12, v16, v17
	v_cvt_pk_bf16_f32 v13, v14, v15
	global_store_dwordx4 v[26:27], v[10:13], off offset:256
	s_nop 1
	v_lshl_add_u64 v[10:11], v[136:137], 0, s[6:7]
	s_mov_b32 s6, 0x58000
	v_pk_mul_f32 v[12:13], v[4:5], v[134:135] op_sel_hi:[1,0]
	v_pk_mul_f32 v[4:5], v[2:3], v[134:135] op_sel_hi:[1,0]
	v_cvt_pk_bf16_f32 v2, v6, v7
	v_add_co_u32_e32 v6, vcc, s6, v136
	v_cvt_pk_bf16_f32 v3, v8, v9
	v_cvt_pk_bf16_f32 v4, v4, v5
	v_cvt_pk_bf16_f32 v5, v12, v13
	v_pk_mul_f32 v[8:9], v[22:23], v[134:135] op_sel_hi:[1,0]
	s_nop 0
	v_addc_co_u32_e32 v7, vcc, 0, v137, vcc
	global_store_dwordx4 v[6:7], v[2:5], off
	v_pk_mul_f32 v[6:7], v[24:25], v[134:135] op_sel_hi:[1,0]
	s_and_b64 vcc, exec, s[4:5]
	v_pk_mul_f32 v[4:5], v[20:21], v[134:135] op_sel_hi:[1,0]
	v_pk_mul_f32 v[2:3], v[18:19], v[134:135] op_sel_hi:[1,0]
	v_mov_b32_e32 v136, v152
	v_mov_b32_e32 v134, v151
	v_cvt_pk_bf16_f32 v2, v2, v3
	v_cvt_pk_bf16_f32 v3, v4, v5
	v_cvt_pk_bf16_f32 v4, v8, v9
	v_cvt_pk_bf16_f32 v5, v6, v7
	global_store_dwordx4 v[10:11], v[2:5], off offset:256
	s_cbranch_vccz .LBB0_1318
	s_waitcnt vmcnt(0)
	s_cmpk_gt_u32 s30, 0xff
	s_cbranch_scc1 .LBB0_1331
	s_barrier
